# attention QK^T and PV segments: LDS fragment reads software-pipelined through 12/7-deep register rings instead of read-wait-mfma chains
# speedup vs baseline: 1.0034x; 1.0034x over previous
; __device__ __forceinline__ void conv_dyn(Frame& F, const Args& a, int limit) {
;     ...
;         int claim = CONV_NCHUNK;
;         if (F.tid == 0 && nid < limit) claim = (int)__hip_atomic_fetch_add(F.ctl + CW_CONV, 1u, RLX_AGENT);
.LBB0_177:
	s_cmpk_lt_i32 s14, 0xc00
	s_cselect_b64 s[4:5], -1, 0
	s_and_b64 s[6:7], s[2:3], s[4:5]
	v_mov_b32_e32 v155, 0x1800
	s_and_saveexec_b64 s[4:5], s[6:7]
	s_cbranch_execz .LBB0_181
	s_mov_b64 s[8:9], exec
	v_mbcnt_lo_u32_b32 v130, s8, 0
	v_mbcnt_hi_u32_b32 v130, s9, v130
	v_cmp_eq_u32_e32 vcc, 0, v130
	s_and_saveexec_b64 s[6:7], vcc
	s_cbranch_execz .LBB0_180
	s_bcnt1_i32_b64 s0, s[8:9]
	v_mov_b32_e32 v131, s0
	global_atomic_add v131, v151, v131, s[76:77] offset:512 sc0
.LBB0_180:
	s_or_b64 exec, exec, s[6:7]
	s_waitcnt vmcnt(0)
	v_readfirstlane_b32 s0, v131
	s_nop 1
	v_add_u32_e32 v155, s0, v130

; __device__ __forceinline__ unsigned f8x4u(float a, float b, float c, float d, float sc) {
;     int w = __builtin_amdgcn_cvt_pk_fp8_f32(a * sc, b * sc, 0, false); return (unsigned)__builtin_amdgcn_cvt_pk_fp8_f32(c * sc, d * sc, w, true);
; }
.LBB0_185:
	s_mov_b64 s[8:9], -1
	s_andn2_b64 vcc, exec, s[6:7]
	v_add_u32_e32 v161, 32, v152
	v_add_u32_e32 v160, 48, v152
	v_add_u32_e32 v159, 64, v152
	v_add_u32_e32 v158, 0x50, v152
	v_add_u32_e32 v157, 0x60, v152
	v_add_u32_e32 v156, 0x70, v152
	s_cbranch_vccnz .LBB0_187
	s_waitcnt vmcnt(19)
	v_mul_f32_e32 v130, s0, v2
	v_mul_f32_e32 v131, s0, v3
	v_mov_b32_e32 v132, v151
	v_cvt_pk_fp8_f32 v132, v130, v131
	s_waitcnt vmcnt(18)
	v_mul_f32_e32 v133, s0, v6
	v_mul_f32_e32 v134, s0, v7
	v_mov_b32_e32 v135, v151
	v_cvt_pk_fp8_f32 v135, v133, v134
	v_mul_f32_e32 v130, s0, v4
	v_mul_f32_e32 v131, s0, v5
	v_cvt_pk_fp8_f32 v132, v130, v131 op_sel:[0,0,1]
	v_mul_f32_e32 v130, s0, v8
	v_mul_f32_e32 v131, s0, v9
	v_cvt_pk_fp8_f32 v135, v130, v131 op_sel:[0,0,1]
	s_waitcnt vmcnt(17)
	v_mul_f32_e32 v130, s0, v10
	v_mul_f32_e32 v131, s0, v11
	v_mov_b32_e32 v133, v151
	v_cvt_pk_fp8_f32 v133, v130, v131
	s_waitcnt vmcnt(16)
	v_mul_f32_e32 v134, s0, v14
	v_mul_f32_e32 v136, s0, v15
	v_mov_b32_e32 v137, v151
	v_cvt_pk_fp8_f32 v137, v134, v136
	v_mul_f32_e32 v130, s0, v12
	v_mul_f32_e32 v131, s0, v13
	v_cvt_pk_fp8_f32 v133, v130, v131 op_sel:[0,0,1]
	v_mul_f32_e32 v130, s0, v16
	v_mul_f32_e32 v131, s0, v17
	v_cvt_pk_fp8_f32 v137, v130, v131 op_sel:[0,0,1]
	s_waitcnt vmcnt(15)
	v_mul_f32_e32 v130, s0, v18
	v_mul_f32_e32 v131, s0, v19
	v_mov_b32_e32 v134, v151
	v_cvt_pk_fp8_f32 v134, v130, v131
	s_waitcnt vmcnt(14)
	v_mul_f32_e32 v136, s0, v22
	v_mul_f32_e32 v138, s0, v23
	v_mov_b32_e32 v139, v151
	v_cvt_pk_fp8_f32 v139, v136, v138
	v_mul_f32_e32 v130, s0, v20
	v_mul_f32_e32 v131, s0, v21
	v_cvt_pk_fp8_f32 v134, v130, v131 op_sel:[0,0,1]
	v_mul_f32_e32 v130, s0, v24
	v_mul_f32_e32 v131, s0, v25
	v_cvt_pk_fp8_f32 v139, v130, v131 op_sel:[0,0,1]
	s_waitcnt vmcnt(13)
	v_mul_f32_e32 v130, s0, v26
	v_mul_f32_e32 v131, s0, v27
	v_mov_b32_e32 v136, v151
	v_cvt_pk_fp8_f32 v136, v130, v131
	s_waitcnt vmcnt(12)
	v_mul_f32_e32 v138, s0, v30
	v_mul_f32_e32 v140, s0, v31
	v_mov_b32_e32 v141, v151
	v_cvt_pk_fp8_f32 v141, v138, v140
	v_mul_f32_e32 v130, s0, v28
	v_mul_f32_e32 v131, s0, v29
	v_cvt_pk_fp8_f32 v136, v130, v131 op_sel:[0,0,1]
	v_mul_f32_e32 v130, s0, v32
	v_mul_f32_e32 v131, s0, v33
	v_cvt_pk_fp8_f32 v141, v130, v131 op_sel:[0,0,1]
	ds_write2st64_b32 v152, v132, v135 offset1:1
	ds_write2_b32 v152, v133, v137 offset0:132 offset1:196
	ds_write2st64_b32 v161, v134, v139 offset0:4 offset1:5
	ds_write2st64_b32 v160, v136, v141 offset0:6 offset1:7
	s_waitcnt vmcnt(11)
	v_mul_f32_e32 v130, s0, v34
	v_mul_f32_e32 v131, s0, v35
	v_mov_b32_e32 v132, v151
	v_cvt_pk_fp8_f32 v132, v130, v131
	s_waitcnt vmcnt(10)
	v_mul_f32_e32 v133, s0, v38
	v_mul_f32_e32 v134, s0, v39
	v_mov_b32_e32 v135, v151
	v_cvt_pk_fp8_f32 v135, v133, v134
	v_mul_f32_e32 v130, s0, v36
	v_mul_f32_e32 v131, s0, v37
	v_cvt_pk_fp8_f32 v132, v130, v131 op_sel:[0,0,1]
	v_mul_f32_e32 v130, s0, v40
	v_mul_f32_e32 v131, s0, v41
	v_cvt_pk_fp8_f32 v135, v130, v131 op_sel:[0,0,1]
	s_waitcnt vmcnt(9)
	v_mul_f32_e32 v130, s0, v42
	v_mul_f32_e32 v131, s0, v43
	v_mov_b32_e32 v133, v151
	v_cvt_pk_fp8_f32 v133, v130, v131
	s_waitcnt vmcnt(8)
	v_mul_f32_e32 v134, s0, v46
	v_mul_f32_e32 v136, s0, v47
	v_mov_b32_e32 v137, v151
	v_cvt_pk_fp8_f32 v137, v134, v136
	v_mul_f32_e32 v130, s0, v44
	v_mul_f32_e32 v131, s0, v45
	v_cvt_pk_fp8_f32 v133, v130, v131 op_sel:[0,0,1]
	v_mul_f32_e32 v130, s0, v48
	v_mul_f32_e32 v131, s0, v49
	v_cvt_pk_fp8_f32 v137, v130, v131 op_sel:[0,0,1]
	s_waitcnt vmcnt(7)
	v_mul_f32_e32 v130, s0, v50
	v_mul_f32_e32 v131, s0, v51
	v_mov_b32_e32 v134, v151
	v_cvt_pk_fp8_f32 v134, v130, v131
	s_waitcnt vmcnt(6)
	v_mul_f32_e32 v136, s0, v54
	v_mul_f32_e32 v138, s0, v55
	v_mov_b32_e32 v139, v151
	v_cvt_pk_fp8_f32 v139, v136, v138
	v_mul_f32_e32 v130, s0, v52
	v_mul_f32_e32 v131, s0, v53
	v_cvt_pk_fp8_f32 v134, v130, v131 op_sel:[0,0,1]
	v_mul_f32_e32 v130, s0, v56
	v_mul_f32_e32 v131, s0, v57
	v_cvt_pk_fp8_f32 v139, v130, v131 op_sel:[0,0,1]
	s_waitcnt vmcnt(5)
	v_mul_f32_e32 v130, s0, v58
	v_mul_f32_e32 v131, s0, v59
	v_mov_b32_e32 v136, v151
	v_cvt_pk_fp8_f32 v136, v130, v131
	s_waitcnt vmcnt(4)
	v_mul_f32_e32 v138, s0, v62
	v_mul_f32_e32 v140, s0, v63
	v_mov_b32_e32 v141, v151
	v_cvt_pk_fp8_f32 v141, v138, v140
	v_mul_f32_e32 v130, s0, v60
	v_mul_f32_e32 v131, s0, v61
	v_cvt_pk_fp8_f32 v136, v130, v131 op_sel:[0,0,1]
	v_mul_f32_e32 v130, s0, v64
	v_mul_f32_e32 v131, s0, v65
	v_cvt_pk_fp8_f32 v141, v130, v131 op_sel:[0,0,1]
	ds_write2st64_b32 v159, v132, v135 offset0:8 offset1:9
	ds_write2st64_b32 v158, v133, v137 offset0:10 offset1:11
	ds_write2st64_b32 v157, v134, v139 offset0:12 offset1:13
	ds_write2st64_b32 v156, v136, v141 offset0:14 offset1:15
	s_waitcnt lgkmcnt(0)
	ds_read2_b32 v[130:131], v149 offset1:8
	ds_read2_b32 v[132:133], v149 offset0:16 offset1:24
	ds_read2_b32 v[136:137], v149 offset0:32 offset1:40
	ds_read2_b32 v[140:141], v149 offset0:48 offset1:56
	ds_read2_b32 v[144:145], v149 offset0:64 offset1:72
	ds_read2_b32 v[162:163], v149 offset0:80 offset1:88
	ds_read2_b32 v[164:165], v149 offset0:96 offset1:104
	ds_read2_b32 v[166:167], v149 offset0:112 offset1:120
	s_waitcnt lgkmcnt(7)
	v_perm_b32 v134, v131, v130, s20
	v_perm_b32 v130, v131, v130, s21
	s_waitcnt lgkmcnt(6)
	v_perm_b32 v131, v133, v132, s20
	v_perm_b32 v132, v133, v132, s21
	s_waitcnt lgkmcnt(0)
	v_perm_b32 v142, v131, v134, s22
	v_perm_b32 v138, v131, v134, s23
	v_perm_b32 v134, v132, v130, s22
	v_perm_b32 v130, v132, v130, s23
	s_waitcnt lgkmcnt(5)
	v_perm_b32 v131, v137, v136, s20
	v_perm_b32 v132, v137, v136, s21
	s_waitcnt lgkmcnt(4)
	v_perm_b32 v133, v141, v140, s20
	v_perm_b32 v136, v141, v140, s21
	v_perm_b32 v143, v133, v131, s22
	v_perm_b32 v139, v133, v131, s23
	v_perm_b32 v135, v136, v132, s22
	v_perm_b32 v131, v136, v132, s23
	s_waitcnt lgkmcnt(3)
	v_perm_b32 v132, v145, v144, s20
	v_perm_b32 v133, v145, v144, s21
	s_waitcnt lgkmcnt(2)
	v_perm_b32 v136, v163, v162, s20
	v_perm_b32 v137, v163, v162, s21
	v_perm_b32 v144, v136, v132, s22
	v_perm_b32 v140, v136, v132, s23
	v_perm_b32 v136, v137, v133, s22
	v_perm_b32 v132, v137, v133, s23
	s_waitcnt lgkmcnt(1)
	v_perm_b32 v133, v165, v164, s20
	v_perm_b32 v150, v165, v164, s21
	s_waitcnt lgkmcnt(0)
	v_perm_b32 v137, v167, v166, s20
	v_perm_b32 v162, v167, v166, s21
	v_perm_b32 v145, v137, v133, s22
	v_perm_b32 v141, v137, v133, s23
	v_perm_b32 v137, v162, v150, s22
	v_perm_b32 v133, v162, v150, s23
	s_mov_b64 s[8:9], 0
; __device__ __forceinline__ unsigned q8x4(float a, float b, float c, float d, float sc) {
;     const float M = 12582912.0f;
;     const unsigned ua = __builtin_bit_cast(unsigned, __builtin_amdgcn_fmed3f(__builtin_fmaf(a, sc, M), M - 127.0f, M + 127.0f)), ub = __builtin_bit_cast(unsigned, __builtin_amdgcn_fmed3f(__builtin_fmaf(b, sc, M), M - 127.0f, M + 127.0f));
;     const unsigned uc = __builtin_bit_cast(unsigned, __builtin_amdgcn_fmed3f(__builtin_fmaf(c, sc, M), M - 127.0f, M + 127.0f)), ud = __builtin_bit_cast(unsigned, __builtin_amdgcn_fmed3f(__builtin_fmaf(d, sc, M), M - 127.0f, M + 127.0f));
;     return __builtin_amdgcn_perm(ub, ua, 0x0c0c0400u) | __builtin_amdgcn_perm(ud, uc, 0x04000c0cu);
.LBB0_187:
	s_andn2_b64 vcc, exec, s[8:9]
	s_cbranch_vccnz .LBB0_189
	s_waitcnt vmcnt(19)
	v_fma_f32 v130, s0, v2, v153
	v_fma_f32 v131, s0, v3, v153
	v_fma_f32 v132, s0, v4, v153
	v_fma_f32 v133, s0, v5, v153
	v_med3_f32 v130, v130, s24, v154
	v_med3_f32 v131, v131, s24, v154
	v_med3_f32 v132, v132, s24, v154
	v_med3_f32 v133, v133, s24, v154
	v_perm_b32 v130, v131, v130, s25
	v_perm_b32 v131, v133, v132, s26
	v_or_b32_e32 v130, v130, v131
	s_waitcnt vmcnt(18)
	v_fma_f32 v131, s0, v6, v153
	v_fma_f32 v132, s0, v7, v153
	v_fma_f32 v133, s0, v8, v153
	v_fma_f32 v134, s0, v9, v153
	v_med3_f32 v131, v131, s24, v154
	v_med3_f32 v132, v132, s24, v154
	v_med3_f32 v133, v133, s24, v154
	v_med3_f32 v134, v134, s24, v154
	v_perm_b32 v131, v132, v131, s25
	v_perm_b32 v132, v134, v133, s26
	v_or_b32_e32 v131, v131, v132
	ds_write2st64_b32 v152, v130, v131 offset1:1
	s_waitcnt vmcnt(17)
	v_fma_f32 v130, s0, v10, v153
	v_fma_f32 v131, s0, v11, v153
	v_fma_f32 v132, s0, v12, v153
	v_fma_f32 v133, s0, v13, v153
	v_med3_f32 v130, v130, s24, v154
	v_med3_f32 v131, v131, s24, v154
	v_med3_f32 v132, v132, s24, v154
	v_med3_f32 v133, v133, s24, v154
	v_perm_b32 v130, v131, v130, s25
	v_perm_b32 v131, v133, v132, s26
	v_or_b32_e32 v130, v130, v131
	s_waitcnt vmcnt(16)
	v_fma_f32 v131, s0, v14, v153
	v_fma_f32 v132, s0, v15, v153
	v_fma_f32 v133, s0, v16, v153
	v_fma_f32 v134, s0, v17, v153
	v_med3_f32 v131, v131, s24, v154
	v_med3_f32 v132, v132, s24, v154
	v_med3_f32 v133, v133, s24, v154
	v_med3_f32 v134, v134, s24, v154
	v_perm_b32 v131, v132, v131, s25
	v_perm_b32 v132, v134, v133, s26
	v_or_b32_e32 v131, v131, v132
	ds_write2_b32 v152, v130, v131 offset0:132 offset1:196
	s_waitcnt vmcnt(15)
	v_fma_f32 v130, s0, v18, v153
	v_fma_f32 v131, s0, v19, v153
	v_fma_f32 v132, s0, v20, v153
	v_fma_f32 v133, s0, v21, v153
	v_med3_f32 v130, v130, s24, v154
	v_med3_f32 v131, v131, s24, v154
	v_med3_f32 v132, v132, s24, v154
	v_med3_f32 v133, v133, s24, v154
	v_perm_b32 v130, v131, v130, s25
	v_perm_b32 v131, v133, v132, s26
	v_or_b32_e32 v130, v130, v131
	s_waitcnt vmcnt(14)
	v_fma_f32 v131, s0, v22, v153
	v_fma_f32 v132, s0, v23, v153
	v_fma_f32 v133, s0, v24, v153
	v_fma_f32 v134, s0, v25, v153
	v_med3_f32 v131, v131, s24, v154
	v_med3_f32 v132, v132, s24, v154
	v_med3_f32 v133, v133, s24, v154
	v_med3_f32 v134, v134, s24, v154
	v_perm_b32 v131, v132, v131, s25
	v_perm_b32 v132, v134, v133, s26
	v_or_b32_e32 v131, v131, v132
	ds_write2st64_b32 v161, v130, v131 offset0:4 offset1:5
	s_waitcnt vmcnt(13)
	v_fma_f32 v130, s0, v26, v153
	v_fma_f32 v131, s0, v27, v153
	v_fma_f32 v132, s0, v28, v153
	v_fma_f32 v133, s0, v29, v153
	v_med3_f32 v130, v130, s24, v154
	v_med3_f32 v131, v131, s24, v154
	v_med3_f32 v132, v132, s24, v154
	v_med3_f32 v133, v133, s24, v154
	v_perm_b32 v130, v131, v130, s25
	v_perm_b32 v131, v133, v132, s26
	v_or_b32_e32 v130, v130, v131
	s_waitcnt vmcnt(12)
	v_fma_f32 v131, s0, v30, v153
	v_fma_f32 v132, s0, v31, v153
	v_fma_f32 v133, s0, v32, v153
	v_fma_f32 v134, s0, v33, v153
	v_med3_f32 v131, v131, s24, v154
	v_med3_f32 v132, v132, s24, v154
	v_med3_f32 v133, v133, s24, v154
	v_med3_f32 v134, v134, s24, v154
	v_perm_b32 v131, v132, v131, s25
	v_perm_b32 v132, v134, v133, s26
	v_or_b32_e32 v131, v131, v132
	ds_write2st64_b32 v160, v130, v131 offset0:6 offset1:7
	s_waitcnt vmcnt(11)
	v_fma_f32 v130, s0, v34, v153
	v_fma_f32 v131, s0, v35, v153
	v_fma_f32 v132, s0, v36, v153
	v_fma_f32 v133, s0, v37, v153
	v_med3_f32 v130, v130, s24, v154
	v_med3_f32 v131, v131, s24, v154
	v_med3_f32 v132, v132, s24, v154
	v_med3_f32 v133, v133, s24, v154
	v_perm_b32 v130, v131, v130, s25
	v_perm_b32 v131, v133, v132, s26
	v_or_b32_e32 v130, v130, v131
	s_waitcnt vmcnt(10)
	v_fma_f32 v131, s0, v38, v153
	v_fma_f32 v132, s0, v39, v153
	v_fma_f32 v133, s0, v40, v153
	v_fma_f32 v134, s0, v41, v153
	v_med3_f32 v131, v131, s24, v154
	v_med3_f32 v132, v132, s24, v154
	v_med3_f32 v133, v133, s24, v154
	v_med3_f32 v134, v134, s24, v154
	v_perm_b32 v131, v132, v131, s25
	v_perm_b32 v132, v134, v133, s26
	v_or_b32_e32 v131, v131, v132
	ds_write2st64_b32 v159, v130, v131 offset0:8 offset1:9
	s_waitcnt vmcnt(9)
	v_fma_f32 v130, s0, v42, v153
	v_fma_f32 v131, s0, v43, v153
	v_fma_f32 v132, s0, v44, v153
	v_fma_f32 v133, s0, v45, v153
	v_med3_f32 v130, v130, s24, v154
	v_med3_f32 v131, v131, s24, v154
	v_med3_f32 v132, v132, s24, v154
	v_med3_f32 v133, v133, s24, v154
	v_perm_b32 v130, v131, v130, s25
	v_perm_b32 v131, v133, v132, s26
	v_or_b32_e32 v130, v130, v131
	s_waitcnt vmcnt(8)
; __device__ __forceinline__ ConvItem conv_decode(const Args& a, int r) {
;     ConvItem c;
;     if (r < CONV_I_GU) { constexpr int PER = (D / 128) * (2 * DFF / 32), NB = 2 * DFF / 32; const int e = r / PER, q = r % PER; c.KK = D; c.NN = 2 * DFF; c.k0 = 128 * (q / NB); c.n0 = 32 * (q % NB); c.d0 = map_wgu(c.n0);
;         c.W = a.wgu + (size_t)e * D * 2 * DFF; c.WT = a.ws + WS_WGU + (size_t)e * 2 * DFF * D; c.scale = SC_WGU; c.i8 = true; }
;     else { r -= CONV_I_GU; constexpr int PER = (DFF / 128) * (D / 32), NB = D / 32; const int e = r / PER, q = r % PER; c.KK = DFF; c.NN = D; c.k0 = 128 * (q / NB); c.n0 = 32 * (q % NB); c.d0 = c.n0;
;         c.W = a.wd + (size_t)e * DFF * D; c.WT = a.ws + WS_WD + (size_t)e * D * DFF; c.scale = SC_WD; c.i8 = false; }
	v_fma_f32 v131, s0, v46, v153
	v_fma_f32 v132, s0, v47, v153
	v_fma_f32 v133, s0, v48, v153
	v_fma_f32 v134, s0, v49, v153
	v_med3_f32 v131, v131, s24, v154
	v_med3_f32 v132, v132, s24, v154
	v_med3_f32 v133, v133, s24, v154
	v_med3_f32 v134, v134, s24, v154
	v_perm_b32 v131, v132, v131, s25
	v_perm_b32 v132, v134, v133, s26
	v_or_b32_e32 v131, v131, v132
	ds_write2st64_b32 v158, v130, v131 offset0:10 offset1:11
	s_waitcnt vmcnt(7)
	v_fma_f32 v130, s0, v50, v153
	v_fma_f32 v131, s0, v51, v153
	v_fma_f32 v132, s0, v52, v153
	v_fma_f32 v133, s0, v53, v153
	v_med3_f32 v130, v130, s24, v154
	v_med3_f32 v131, v131, s24, v154
	v_med3_f32 v132, v132, s24, v154
	v_med3_f32 v133, v133, s24, v154
	v_perm_b32 v130, v131, v130, s25
	v_perm_b32 v131, v133, v132, s26
	v_or_b32_e32 v130, v130, v131
	s_waitcnt vmcnt(6)
	v_fma_f32 v131, s0, v54, v153
	v_fma_f32 v132, s0, v55, v153
	v_fma_f32 v133, s0, v56, v153
	v_fma_f32 v134, s0, v57, v153
	v_med3_f32 v131, v131, s24, v154
	v_med3_f32 v132, v132, s24, v154
	v_med3_f32 v133, v133, s24, v154
	v_med3_f32 v134, v134, s24, v154
	v_perm_b32 v131, v132, v131, s25
	v_perm_b32 v132, v134, v133, s26
	v_or_b32_e32 v131, v131, v132
	ds_write2st64_b32 v157, v130, v131 offset0:12 offset1:13
	s_waitcnt vmcnt(5)
	v_fma_f32 v130, s0, v58, v153
	v_fma_f32 v131, s0, v59, v153
	v_fma_f32 v132, s0, v60, v153
	v_fma_f32 v133, s0, v61, v153
	v_med3_f32 v130, v130, s24, v154
	v_med3_f32 v131, v131, s24, v154
	v_med3_f32 v132, v132, s24, v154
	v_med3_f32 v133, v133, s24, v154
	v_perm_b32 v130, v131, v130, s25
	v_perm_b32 v131, v133, v132, s26
	v_or_b32_e32 v130, v130, v131
	s_waitcnt vmcnt(4)
	v_fma_f32 v131, s0, v62, v153
	v_fma_f32 v132, s0, v63, v153
	v_fma_f32 v133, s0, v64, v153
	v_fma_f32 v134, s0, v65, v153
	v_med3_f32 v131, v131, s24, v154
	v_med3_f32 v132, v132, s24, v154
	v_med3_f32 v133, v133, s24, v154
	v_med3_f32 v134, v134, s24, v154
	v_perm_b32 v131, v132, v131, s25
	v_perm_b32 v132, v134, v133, s26
	v_or_b32_e32 v131, v131, v132
	ds_write2st64_b32 v156, v130, v131 offset0:14 offset1:15
	s_waitcnt lgkmcnt(0)
	ds_read2_b32 v[130:131], v149 offset1:8
	ds_read2_b32 v[132:133], v149 offset0:16 offset1:24
	ds_read2_b32 v[136:137], v149 offset0:32 offset1:40
	ds_read2_b32 v[140:141], v149 offset0:48 offset1:56
	ds_read2_b32 v[144:145], v149 offset0:64 offset1:72
	ds_read2_b32 v[162:163], v149 offset0:80 offset1:88
	ds_read2_b32 v[164:165], v149 offset0:96 offset1:104
	ds_read2_b32 v[166:167], v149 offset0:112 offset1:120
	s_waitcnt lgkmcnt(7)
	v_perm_b32 v134, v131, v130, s20
	v_perm_b32 v130, v131, v130, s21
	s_waitcnt lgkmcnt(6)
	v_perm_b32 v131, v133, v132, s20
	v_perm_b32 v132, v133, v132, s21
	s_waitcnt lgkmcnt(0)
	v_perm_b32 v142, v131, v134, s22
	v_perm_b32 v138, v131, v134, s23
	v_perm_b32 v134, v132, v130, s22
	v_perm_b32 v130, v132, v130, s23
	s_waitcnt lgkmcnt(5)
	v_perm_b32 v131, v137, v136, s20
	v_perm_b32 v132, v137, v136, s21
	s_waitcnt lgkmcnt(4)
	v_perm_b32 v133, v141, v140, s20
	v_perm_b32 v136, v141, v140, s21
	v_perm_b32 v143, v133, v131, s22
	v_perm_b32 v139, v133, v131, s23
	v_perm_b32 v135, v136, v132, s22
	v_perm_b32 v131, v136, v132, s23
	s_waitcnt lgkmcnt(3)
	v_perm_b32 v132, v145, v144, s20
	v_perm_b32 v133, v145, v144, s21
	s_waitcnt lgkmcnt(2)
	v_perm_b32 v136, v163, v162, s20
	v_perm_b32 v137, v163, v162, s21
	v_perm_b32 v144, v136, v132, s22
	v_perm_b32 v140, v136, v132, s23
	v_perm_b32 v136, v137, v133, s22
	v_perm_b32 v132, v137, v133, s23
	s_waitcnt lgkmcnt(1)
	v_perm_b32 v133, v165, v164, s20
	v_perm_b32 v150, v165, v164, s21
	s_waitcnt lgkmcnt(0)
	v_perm_b32 v137, v167, v166, s20
	v_perm_b32 v162, v167, v166, s21
	v_perm_b32 v145, v137, v133, s22
	v_perm_b32 v141, v137, v133, s23
	v_perm_b32 v137, v162, v150, s22
	v_perm_b32 v133, v162, v150, s23
.LBB0_189:
	s_lshl_b32 s28, s14, 4
	s_add_i32 s28, s28, s15
	s_ashr_i32 s0, s10, 31
	v_add_u32_e32 v162, s11, v148
	s_add_u32 s4, s4, s10
	s_addc_u32 s5, s5, s0
	v_ashrrev_i32_e32 v163, 31, v162
	v_lshl_add_u64 v[164:165], s[4:5], 0, v[146:147]
	v_lshlrev_b64 v[162:163], 11, v[162:163]
	v_lshl_add_u64 v[162:163], v[164:165], 0, v[162:163]
	s_cmpk_lt_i32 s14, 0x1800
	global_store_dwordx4 v[162:163], v[142:145], off nt
	global_store_dwordx4 v[162:163], v[138:141], off offset:2048 nt
	s_cselect_b64 s[6:7], -1, 0
	s_cmpk_gt_i32 s14, 0x17ff
	v_add_co_u32_e32 v138, vcc, 0x1000, v162
	s_cselect_b64 s[4:5], -1, 0
	s_nop 0
	v_addc_co_u32_e32 v139, vcc, 0, v163, vcc
	s_and_b64 vcc, exec, s[4:5]
	global_store_dwordx4 v[138:139], v[134:137], off nt
	global_store_dwordx4 v[138:139], v[130:133], off offset:2048 nt
	s_cbranch_vccnz .LBB0_195
	s_cmp_gt_i32 s28, 0xffff
	s_mov_b64 s[12:13], -1
	s_cbranch_scc0 .LBB0_192
	s_add_i32 s0, s28, 0xffff0000
	s_lshl_b32 s8, s28, 1
	s_lshr_b32 s0, s0, 10
	s_and_b32 s9, s8, 0x780
	s_lshl_b32 s8, s28, 5
	s_and_b32 s8, s8, 0x7c0
	s_lshl_b64 s[10:11], s[0:1], 24
	s_add_u32 s10, s86, s10
	s_addc_u32 s11, s87, s11
	s_mov_b64 s[12:13], 0

; #define FP8_ITEM_LOAD(rv, W, N, k0, n0) do { const float* wsrc_ = (W) + (size_t)((k0) + (lane >> 3)) * (N) + (n0) + 4 * (lane & 7); \
;         _Pragma("unroll") for (int i_ = 0; i_ < 16; ++i_) rv[i_] = __builtin_nontemporal_load((const f32x4*)(wsrc_ + (size_t)(8 * i_) * (N))); } while (0)
; __device__ __forceinline__ void conv_dyn(Frame& F, const Args& a, int limit) {
;     ...
;         if (nid < CONV_NCHUNK) { const ConvItem c = conv_decode(a, n0); FP8_ITEM_LOAD(ra, c.W, c.NN, c.k0, c.n0); }
.LBB0_194:
	s_waitcnt vmcnt(23)
	v_or_b32_e32 v2, s9, v1
	v_mul_hi_i32_i24_e32 v3, s12, v2
	v_mul_i32_i24_e32 v2, s12, v2
	v_lshl_add_u64 v[2:3], v[2:3], 2, s[10:11]
	s_ashr_i32 s9, s8, 31
	v_lshl_add_u64 v[2:3], s[8:9], 2, v[2:3]
	v_lshlrev_b32_e32 v150, 2, v148
	v_lshl_add_u64 v[2:3], v[2:3], 0, v[150:151]
	s_lshl_b32 s0, s12, 5
	s_waitcnt vmcnt(21)
	v_lshl_add_u64 v[10:11], v[2:3], 0, s[0:1]
	global_load_dwordx4 v[2:5], v[2:3], off nt
	s_nop 0
	global_load_dwordx4 v[6:9], v[10:11], off nt
	v_lshl_add_u64 v[10:11], v[10:11], 0, s[0:1]
	s_waitcnt vmcnt(21)
	v_lshl_add_u64 v[18:19], v[10:11], 0, s[0:1]
	global_load_dwordx4 v[10:13], v[10:11], off nt
	s_nop 0
	global_load_dwordx4 v[14:17], v[18:19], off nt
	v_lshl_add_u64 v[18:19], v[18:19], 0, s[0:1]
	s_waitcnt vmcnt(21)
	v_lshl_add_u64 v[26:27], v[18:19], 0, s[0:1]
	global_load_dwordx4 v[18:21], v[18:19], off nt
	s_nop 0
	global_load_dwordx4 v[22:25], v[26:27], off nt
	v_lshl_add_u64 v[26:27], v[26:27], 0, s[0:1]
	s_waitcnt vmcnt(21)
	v_lshl_add_u64 v[34:35], v[26:27], 0, s[0:1]
	s_waitcnt vmcnt(20)
	v_lshl_add_u64 v[38:39], v[34:35], 0, s[0:1]
	s_waitcnt vmcnt(19)
	v_lshl_add_u64 v[42:43], v[38:39], 0, s[0:1]
	s_waitcnt vmcnt(18)
	v_lshl_add_u64 v[46:47], v[42:43], 0, s[0:1]
	s_waitcnt vmcnt(17)
	v_lshl_add_u64 v[50:51], v[46:47], 0, s[0:1]
	s_waitcnt vmcnt(16)
	v_lshl_add_u64 v[54:55], v[50:51], 0, s[0:1]
	s_waitcnt vmcnt(15)
	v_lshl_add_u64 v[58:59], v[54:55], 0, s[0:1]
	s_waitcnt vmcnt(14)
	v_lshl_add_u64 v[62:63], v[58:59], 0, s[0:1]
	global_load_dwordx4 v[26:29], v[26:27], off nt
	s_nop 0
	global_load_dwordx4 v[30:33], v[34:35], off nt
	s_nop 0
	global_load_dwordx4 v[34:37], v[38:39], off nt
	s_nop 0
	global_load_dwordx4 v[38:41], v[42:43], off nt
	s_nop 0
	global_load_dwordx4 v[42:45], v[46:47], off nt
	s_nop 0
	global_load_dwordx4 v[46:49], v[50:51], off nt
	s_nop 0
	global_load_dwordx4 v[50:53], v[54:55], off nt
	s_nop 0
	global_load_dwordx4 v[54:57], v[58:59], off nt
	s_nop 0
	global_load_dwordx4 v[58:61], v[62:63], off nt
	v_lshl_add_u64 v[62:63], v[62:63], 0, s[0:1]
	global_load_dwordx4 v[62:65], v[62:63], off nt

; __device__ __forceinline__ unsigned f8x4u(float a, float b, float c, float d, float sc) {
;     int w = __builtin_amdgcn_cvt_pk_fp8_f32(a * sc, b * sc, 0, false); return (unsigned)__builtin_amdgcn_cvt_pk_fp8_f32(c * sc, d * sc, w, true);
; }
.LBB0_199:
	s_andn2_b64 vcc, exec, s[10:11]
	s_mov_b64 s[10:11], -1
	s_cbranch_vccnz .LBB0_201
	s_waitcnt vmcnt(19)
	v_mul_f32_e32 v130, s0, v66
	v_mul_f32_e32 v131, s0, v67
	v_mov_b32_e32 v132, v151
	v_cvt_pk_fp8_f32 v132, v130, v131
	s_waitcnt vmcnt(18)
	v_mul_f32_e32 v133, s0, v70
	v_mul_f32_e32 v134, s0, v71
	v_mov_b32_e32 v135, v151
	v_cvt_pk_fp8_f32 v135, v133, v134
	v_mul_f32_e32 v130, s0, v68
	v_mul_f32_e32 v131, s0, v69
	v_cvt_pk_fp8_f32 v132, v130, v131 op_sel:[0,0,1]
	v_mul_f32_e32 v130, s0, v72
	v_mul_f32_e32 v131, s0, v73
	v_cvt_pk_fp8_f32 v135, v130, v131 op_sel:[0,0,1]
	s_waitcnt vmcnt(17)
	v_mul_f32_e32 v130, s0, v74
	v_mul_f32_e32 v131, s0, v75
	v_mov_b32_e32 v133, v151
	v_cvt_pk_fp8_f32 v133, v130, v131
	s_waitcnt vmcnt(16)
	v_mul_f32_e32 v134, s0, v78
	v_mul_f32_e32 v136, s0, v79
	v_mov_b32_e32 v137, v151
	v_cvt_pk_fp8_f32 v137, v134, v136
	v_mul_f32_e32 v130, s0, v76
	v_mul_f32_e32 v131, s0, v77
	v_cvt_pk_fp8_f32 v133, v130, v131 op_sel:[0,0,1]
	v_mul_f32_e32 v130, s0, v80
	v_mul_f32_e32 v131, s0, v81
	v_cvt_pk_fp8_f32 v137, v130, v131 op_sel:[0,0,1]
	s_waitcnt vmcnt(15)
	v_mul_f32_e32 v130, s0, v82
	v_mul_f32_e32 v131, s0, v83
	v_mov_b32_e32 v134, v151
	v_cvt_pk_fp8_f32 v134, v130, v131
	s_waitcnt vmcnt(14)
	v_mul_f32_e32 v136, s0, v86
	v_mul_f32_e32 v138, s0, v87
	v_mov_b32_e32 v139, v151
	v_cvt_pk_fp8_f32 v139, v136, v138
	v_mul_f32_e32 v130, s0, v84
	v_mul_f32_e32 v131, s0, v85
	v_cvt_pk_fp8_f32 v134, v130, v131 op_sel:[0,0,1]
	v_mul_f32_e32 v130, s0, v88
	v_mul_f32_e32 v131, s0, v89
	v_cvt_pk_fp8_f32 v139, v130, v131 op_sel:[0,0,1]
	s_waitcnt vmcnt(13)
	v_mul_f32_e32 v130, s0, v90
	v_mul_f32_e32 v131, s0, v91
	v_mov_b32_e32 v136, v151
	v_cvt_pk_fp8_f32 v136, v130, v131
	s_waitcnt vmcnt(12)
	v_mul_f32_e32 v138, s0, v94
	v_mul_f32_e32 v140, s0, v95
	v_mov_b32_e32 v141, v151
	v_cvt_pk_fp8_f32 v141, v138, v140
	v_mul_f32_e32 v130, s0, v92
	v_mul_f32_e32 v131, s0, v93
	v_cvt_pk_fp8_f32 v136, v130, v131 op_sel:[0,0,1]
	v_mul_f32_e32 v130, s0, v96
	v_mul_f32_e32 v131, s0, v97
	v_cvt_pk_fp8_f32 v141, v130, v131 op_sel:[0,0,1]
	ds_write2st64_b32 v152, v132, v135 offset1:1
	ds_write2_b32 v152, v133, v137 offset0:132 offset1:196
	ds_write2st64_b32 v161, v134, v139 offset0:4 offset1:5
	ds_write2st64_b32 v160, v136, v141 offset0:6 offset1:7
	s_waitcnt vmcnt(11)
	v_mul_f32_e32 v130, s0, v98
	v_mul_f32_e32 v131, s0, v99
	v_mov_b32_e32 v132, v151
	v_cvt_pk_fp8_f32 v132, v130, v131
	s_waitcnt vmcnt(10)
	v_mul_f32_e32 v133, s0, v102
	v_mul_f32_e32 v134, s0, v103
	v_mov_b32_e32 v135, v151
	v_cvt_pk_fp8_f32 v135, v133, v134
	v_mul_f32_e32 v130, s0, v100
	v_mul_f32_e32 v131, s0, v101
	v_cvt_pk_fp8_f32 v132, v130, v131 op_sel:[0,0,1]
	v_mul_f32_e32 v130, s0, v104
	v_mul_f32_e32 v131, s0, v105
	v_cvt_pk_fp8_f32 v135, v130, v131 op_sel:[0,0,1]
	s_waitcnt vmcnt(9)
	v_mul_f32_e32 v130, s0, v106
	v_mul_f32_e32 v131, s0, v107
	v_mov_b32_e32 v133, v151
	v_cvt_pk_fp8_f32 v133, v130, v131
	s_waitcnt vmcnt(8)
	v_mul_f32_e32 v134, s0, v110
	v_mul_f32_e32 v136, s0, v111
	v_mov_b32_e32 v137, v151
	v_cvt_pk_fp8_f32 v137, v134, v136
	v_mul_f32_e32 v130, s0, v108
	v_mul_f32_e32 v131, s0, v109
	v_cvt_pk_fp8_f32 v133, v130, v131 op_sel:[0,0,1]
	v_mul_f32_e32 v130, s0, v112
	v_mul_f32_e32 v131, s0, v113
	v_cvt_pk_fp8_f32 v137, v130, v131 op_sel:[0,0,1]
	s_waitcnt vmcnt(7)
	v_mul_f32_e32 v130, s0, v114
	v_mul_f32_e32 v131, s0, v115
	v_mov_b32_e32 v134, v151
	v_cvt_pk_fp8_f32 v134, v130, v131
	s_waitcnt vmcnt(6)
	v_mul_f32_e32 v136, s0, v118
	v_mul_f32_e32 v138, s0, v119
	v_mov_b32_e32 v139, v151
	v_cvt_pk_fp8_f32 v139, v136, v138
	v_mul_f32_e32 v130, s0, v116
	v_mul_f32_e32 v131, s0, v117
	v_cvt_pk_fp8_f32 v134, v130, v131 op_sel:[0,0,1]
	v_mul_f32_e32 v130, s0, v120
	v_mul_f32_e32 v131, s0, v121
	v_cvt_pk_fp8_f32 v139, v130, v131 op_sel:[0,0,1]
	s_waitcnt vmcnt(5)
	v_mul_f32_e32 v130, s0, v122
	v_mul_f32_e32 v131, s0, v123
	v_mov_b32_e32 v136, v151
	v_cvt_pk_fp8_f32 v136, v130, v131
	s_waitcnt vmcnt(4)
	v_mul_f32_e32 v138, s0, v126
	v_mul_f32_e32 v140, s0, v127
	v_mov_b32_e32 v141, v151
	v_cvt_pk_fp8_f32 v141, v138, v140
	v_mul_f32_e32 v130, s0, v124
	v_mul_f32_e32 v131, s0, v125
	v_cvt_pk_fp8_f32 v136, v130, v131 op_sel:[0,0,1]
	v_mul_f32_e32 v130, s0, v128
	v_mul_f32_e32 v131, s0, v129
	v_cvt_pk_fp8_f32 v141, v130, v131 op_sel:[0,0,1]
	ds_write2st64_b32 v159, v132, v135 offset0:8 offset1:9
	ds_write2st64_b32 v158, v133, v137 offset0:10 offset1:11
	ds_write2st64_b32 v157, v134, v139 offset0:12 offset1:13
	ds_write2st64_b32 v156, v136, v141 offset0:14 offset1:15
	s_waitcnt lgkmcnt(0)
	ds_read2_b32 v[130:131], v149 offset1:8
	ds_read2_b32 v[132:133], v149 offset0:16 offset1:24
	ds_read2_b32 v[136:137], v149 offset0:32 offset1:40
	ds_read2_b32 v[140:141], v149 offset0:48 offset1:56
	ds_read2_b32 v[144:145], v149 offset0:64 offset1:72
	ds_read2_b32 v[162:163], v149 offset0:80 offset1:88
	ds_read2_b32 v[164:165], v149 offset0:96 offset1:104
	ds_read2_b32 v[166:167], v149 offset0:112 offset1:120
	s_waitcnt lgkmcnt(7)
	v_perm_b32 v134, v131, v130, s20
	v_perm_b32 v130, v131, v130, s21
	s_waitcnt lgkmcnt(6)
	v_perm_b32 v131, v133, v132, s20
	v_perm_b32 v132, v133, v132, s21
	s_waitcnt lgkmcnt(0)
	v_perm_b32 v142, v131, v134, s22
	v_perm_b32 v138, v131, v134, s23
	v_perm_b32 v134, v132, v130, s22
	v_perm_b32 v130, v132, v130, s23
	s_waitcnt lgkmcnt(5)
	v_perm_b32 v131, v137, v136, s20
	v_perm_b32 v132, v137, v136, s21
	s_waitcnt lgkmcnt(4)
	v_perm_b32 v133, v141, v140, s20
	v_perm_b32 v136, v141, v140, s21
	v_perm_b32 v143, v133, v131, s22
	v_perm_b32 v139, v133, v131, s23
	v_perm_b32 v135, v136, v132, s22
	v_perm_b32 v131, v136, v132, s23
	s_waitcnt lgkmcnt(3)
	v_perm_b32 v132, v145, v144, s20
	v_perm_b32 v133, v145, v144, s21
	s_waitcnt lgkmcnt(2)
	v_perm_b32 v136, v163, v162, s20
	v_perm_b32 v137, v163, v162, s21
	v_perm_b32 v144, v136, v132, s22
	v_perm_b32 v140, v136, v132, s23
	v_perm_b32 v136, v137, v133, s22
	v_perm_b32 v132, v137, v133, s23
	s_waitcnt lgkmcnt(1)
	v_perm_b32 v133, v165, v164, s20
	v_perm_b32 v150, v165, v164, s21
	s_waitcnt lgkmcnt(0)
	v_perm_b32 v137, v167, v166, s20
	v_perm_b32 v162, v167, v166, s21
	v_perm_b32 v145, v137, v133, s22
	v_perm_b32 v141, v137, v133, s23
	v_perm_b32 v137, v162, v150, s22
	v_perm_b32 v133, v162, v150, s23
	s_cbranch_execz .LBB0_202
	s_branch .LBB0_203

; __device__ __forceinline__ unsigned q8x4(float a, float b, float c, float d, float sc) {
;     const float M = 12582912.0f;
;     const unsigned ua = __builtin_bit_cast(unsigned, __builtin_amdgcn_fmed3f(__builtin_fmaf(a, sc, M), M - 127.0f, M + 127.0f)), ub = __builtin_bit_cast(unsigned, __builtin_amdgcn_fmed3f(__builtin_fmaf(b, sc, M), M - 127.0f, M + 127.0f));
;     const unsigned uc = __builtin_bit_cast(unsigned, __builtin_amdgcn_fmed3f(__builtin_fmaf(c, sc, M), M - 127.0f, M + 127.0f)), ud = __builtin_bit_cast(unsigned, __builtin_amdgcn_fmed3f(__builtin_fmaf(d, sc, M), M - 127.0f, M + 127.0f));
;     return __builtin_amdgcn_perm(ub, ua, 0x0c0c0400u) | __builtin_amdgcn_perm(ud, uc, 0x04000c0cu);
.LBB0_202:
	s_waitcnt vmcnt(19)
	v_fma_f32 v130, s0, v66, v153
	v_fma_f32 v131, s0, v67, v153
	v_fma_f32 v132, s0, v68, v153
	v_fma_f32 v133, s0, v69, v153
	v_med3_f32 v130, v130, s24, v154
	v_med3_f32 v131, v131, s24, v154
	v_med3_f32 v132, v132, s24, v154
	v_med3_f32 v133, v133, s24, v154
	v_perm_b32 v130, v131, v130, s25
	v_perm_b32 v131, v133, v132, s26
	v_or_b32_e32 v130, v130, v131
	s_waitcnt vmcnt(18)
	v_fma_f32 v131, s0, v70, v153
	v_fma_f32 v132, s0, v71, v153
	v_fma_f32 v133, s0, v72, v153
	v_fma_f32 v134, s0, v73, v153
	v_med3_f32 v131, v131, s24, v154
	v_med3_f32 v132, v132, s24, v154
	v_med3_f32 v133, v133, s24, v154
	v_med3_f32 v134, v134, s24, v154
	v_perm_b32 v131, v132, v131, s25
	v_perm_b32 v132, v134, v133, s26
	v_or_b32_e32 v131, v131, v132
	ds_write2st64_b32 v152, v130, v131 offset1:1
	s_waitcnt vmcnt(17)
	v_fma_f32 v130, s0, v74, v153
	v_fma_f32 v131, s0, v75, v153
	v_fma_f32 v132, s0, v76, v153
	v_fma_f32 v133, s0, v77, v153
	v_med3_f32 v130, v130, s24, v154
	v_med3_f32 v131, v131, s24, v154
	v_med3_f32 v132, v132, s24, v154
	v_med3_f32 v133, v133, s24, v154
	v_perm_b32 v130, v131, v130, s25
	v_perm_b32 v131, v133, v132, s26
	v_or_b32_e32 v130, v130, v131
	s_waitcnt vmcnt(16)
	v_fma_f32 v131, s0, v78, v153
	v_fma_f32 v132, s0, v79, v153
	v_fma_f32 v133, s0, v80, v153
	v_fma_f32 v134, s0, v81, v153
	v_med3_f32 v131, v131, s24, v154
	v_med3_f32 v132, v132, s24, v154
	v_med3_f32 v133, v133, s24, v154
	v_med3_f32 v134, v134, s24, v154
	v_perm_b32 v131, v132, v131, s25
	v_perm_b32 v132, v134, v133, s26
	v_or_b32_e32 v131, v131, v132
	ds_write2_b32 v152, v130, v131 offset0:132 offset1:196
	s_waitcnt vmcnt(15)
	v_fma_f32 v130, s0, v82, v153
	v_fma_f32 v131, s0, v83, v153
	v_fma_f32 v132, s0, v84, v153
	v_fma_f32 v133, s0, v85, v153
	v_med3_f32 v130, v130, s24, v154
	v_med3_f32 v131, v131, s24, v154
	v_med3_f32 v132, v132, s24, v154
	v_med3_f32 v133, v133, s24, v154
	v_perm_b32 v130, v131, v130, s25
	v_perm_b32 v131, v133, v132, s26
	v_or_b32_e32 v130, v130, v131
	s_waitcnt vmcnt(14)
	v_fma_f32 v131, s0, v86, v153
	v_fma_f32 v132, s0, v87, v153
	v_fma_f32 v133, s0, v88, v153
	v_fma_f32 v134, s0, v89, v153
	v_med3_f32 v131, v131, s24, v154
	v_med3_f32 v132, v132, s24, v154
	v_med3_f32 v133, v133, s24, v154
	v_med3_f32 v134, v134, s24, v154
	v_perm_b32 v131, v132, v131, s25
	v_perm_b32 v132, v134, v133, s26
	v_or_b32_e32 v131, v131, v132
	ds_write2st64_b32 v161, v130, v131 offset0:4 offset1:5
	s_waitcnt vmcnt(13)
	v_fma_f32 v130, s0, v90, v153
	v_fma_f32 v131, s0, v91, v153
	v_fma_f32 v132, s0, v92, v153
	v_fma_f32 v133, s0, v93, v153
	v_med3_f32 v130, v130, s24, v154
	v_med3_f32 v131, v131, s24, v154
	v_med3_f32 v132, v132, s24, v154
	v_med3_f32 v133, v133, s24, v154
	v_perm_b32 v130, v131, v130, s25
	v_perm_b32 v131, v133, v132, s26
	v_or_b32_e32 v130, v130, v131
	s_waitcnt vmcnt(12)
	v_fma_f32 v131, s0, v94, v153
	v_fma_f32 v132, s0, v95, v153
	v_fma_f32 v133, s0, v96, v153
	v_fma_f32 v134, s0, v97, v153
	v_med3_f32 v131, v131, s24, v154
	v_med3_f32 v132, v132, s24, v154
	v_med3_f32 v133, v133, s24, v154
	v_med3_f32 v134, v134, s24, v154
	v_perm_b32 v131, v132, v131, s25
	v_perm_b32 v132, v134, v133, s26
	v_or_b32_e32 v131, v131, v132
	ds_write2st64_b32 v160, v130, v131 offset0:6 offset1:7
	s_waitcnt vmcnt(11)
	v_fma_f32 v130, s0, v98, v153
	v_fma_f32 v131, s0, v99, v153
	v_fma_f32 v132, s0, v100, v153
	v_fma_f32 v133, s0, v101, v153
	v_med3_f32 v130, v130, s24, v154
	v_med3_f32 v131, v131, s24, v154
	v_med3_f32 v132, v132, s24, v154
	v_med3_f32 v133, v133, s24, v154
	v_perm_b32 v130, v131, v130, s25
	v_perm_b32 v131, v133, v132, s26
	v_or_b32_e32 v130, v130, v131
	s_waitcnt vmcnt(10)
	v_fma_f32 v131, s0, v102, v153
	v_fma_f32 v132, s0, v103, v153
	v_fma_f32 v133, s0, v104, v153
	v_fma_f32 v134, s0, v105, v153
	v_med3_f32 v131, v131, s24, v154
	v_med3_f32 v132, v132, s24, v154
	v_med3_f32 v133, v133, s24, v154
	v_med3_f32 v134, v134, s24, v154
	v_perm_b32 v131, v132, v131, s25
	v_perm_b32 v132, v134, v133, s26
	v_or_b32_e32 v131, v131, v132
	ds_write2st64_b32 v159, v130, v131 offset0:8 offset1:9
	s_waitcnt vmcnt(9)
	v_fma_f32 v130, s0, v106, v153
	v_fma_f32 v131, s0, v107, v153
	v_fma_f32 v132, s0, v108, v153
	v_fma_f32 v133, s0, v109, v153
	v_med3_f32 v130, v130, s24, v154
	v_med3_f32 v131, v131, s24, v154
	v_med3_f32 v132, v132, s24, v154
	v_med3_f32 v133, v133, s24, v154
	v_perm_b32 v130, v131, v130, s25
	v_perm_b32 v131, v133, v132, s26
	v_or_b32_e32 v130, v130, v131
	s_waitcnt vmcnt(8)
; __device__ __forceinline__ ConvItem conv_decode(const Args& a, int r) {
;     ConvItem c;
;     if (r < CONV_I_GU) { constexpr int PER = (D / 128) * (2 * DFF / 32), NB = 2 * DFF / 32; const int e = r / PER, q = r % PER; c.KK = D; c.NN = 2 * DFF; c.k0 = 128 * (q / NB); c.n0 = 32 * (q % NB); c.d0 = map_wgu(c.n0);
;         c.W = a.wgu + (size_t)e * D * 2 * DFF; c.WT = a.ws + WS_WGU + (size_t)e * 2 * DFF * D; c.scale = SC_WGU; c.i8 = true; }
;     else { r -= CONV_I_GU; constexpr int PER = (DFF / 128) * (D / 32), NB = D / 32; const int e = r / PER, q = r % PER; c.KK = DFF; c.NN = D; c.k0 = 128 * (q / NB); c.n0 = 32 * (q % NB); c.d0 = c.n0;
;         c.W = a.wd + (size_t)e * DFF * D; c.WT = a.ws + WS_WD + (size_t)e * D * DFF; c.scale = SC_WD; c.i8 = false; }
	v_fma_f32 v131, s0, v110, v153
	v_fma_f32 v132, s0, v111, v153
	v_fma_f32 v133, s0, v112, v153
	v_fma_f32 v134, s0, v113, v153
	v_med3_f32 v131, v131, s24, v154
	v_med3_f32 v132, v132, s24, v154
	v_med3_f32 v133, v133, s24, v154
	v_med3_f32 v134, v134, s24, v154
	v_perm_b32 v131, v132, v131, s25
	v_perm_b32 v132, v134, v133, s26
	v_or_b32_e32 v131, v131, v132
	ds_write2st64_b32 v158, v130, v131 offset0:10 offset1:11
	s_waitcnt vmcnt(7)
	v_fma_f32 v130, s0, v114, v153
	v_fma_f32 v131, s0, v115, v153
	v_fma_f32 v132, s0, v116, v153
	v_fma_f32 v133, s0, v117, v153
	v_med3_f32 v130, v130, s24, v154
	v_med3_f32 v131, v131, s24, v154
	v_med3_f32 v132, v132, s24, v154
	v_med3_f32 v133, v133, s24, v154
	v_perm_b32 v130, v131, v130, s25
	v_perm_b32 v131, v133, v132, s26
	v_or_b32_e32 v130, v130, v131
	s_waitcnt vmcnt(6)
	v_fma_f32 v131, s0, v118, v153
	v_fma_f32 v132, s0, v119, v153
	v_fma_f32 v133, s0, v120, v153
	v_fma_f32 v134, s0, v121, v153
	v_med3_f32 v131, v131, s24, v154
	v_med3_f32 v132, v132, s24, v154
	v_med3_f32 v133, v133, s24, v154
	v_med3_f32 v134, v134, s24, v154
	v_perm_b32 v131, v132, v131, s25
	v_perm_b32 v132, v134, v133, s26
	v_or_b32_e32 v131, v131, v132
	ds_write2st64_b32 v157, v130, v131 offset0:12 offset1:13
	s_waitcnt vmcnt(5)
	v_fma_f32 v130, s0, v122, v153
	v_fma_f32 v131, s0, v123, v153
	v_fma_f32 v132, s0, v124, v153
	v_fma_f32 v133, s0, v125, v153
	v_med3_f32 v130, v130, s24, v154
	v_med3_f32 v131, v131, s24, v154
	v_med3_f32 v132, v132, s24, v154
	v_med3_f32 v133, v133, s24, v154
	v_perm_b32 v130, v131, v130, s25
	v_perm_b32 v131, v133, v132, s26
	v_or_b32_e32 v130, v130, v131
	s_waitcnt vmcnt(4)
	v_fma_f32 v131, s0, v126, v153
	v_fma_f32 v132, s0, v127, v153
	v_fma_f32 v133, s0, v128, v153
	v_fma_f32 v134, s0, v129, v153
	v_med3_f32 v131, v131, s24, v154
	v_med3_f32 v132, v132, s24, v154
	v_med3_f32 v133, v133, s24, v154
	v_med3_f32 v134, v134, s24, v154
	v_perm_b32 v131, v132, v131, s25
	v_perm_b32 v132, v134, v133, s26
	v_or_b32_e32 v131, v131, v132
	ds_write2st64_b32 v156, v130, v131 offset0:14 offset1:15
	s_waitcnt lgkmcnt(0)
	ds_read2_b32 v[130:131], v149 offset1:8
	ds_read2_b32 v[132:133], v149 offset0:16 offset1:24
	ds_read2_b32 v[136:137], v149 offset0:32 offset1:40
	ds_read2_b32 v[140:141], v149 offset0:48 offset1:56
	ds_read2_b32 v[144:145], v149 offset0:64 offset1:72
	ds_read2_b32 v[156:157], v149 offset0:80 offset1:88
	ds_read2_b32 v[158:159], v149 offset0:96 offset1:104
	ds_read2_b32 v[160:161], v149 offset0:112 offset1:120
	s_waitcnt lgkmcnt(7)
	v_perm_b32 v134, v131, v130, s20
	v_perm_b32 v130, v131, v130, s21
	s_waitcnt lgkmcnt(6)
	v_perm_b32 v131, v133, v132, s20
	v_perm_b32 v132, v133, v132, s21
	s_waitcnt lgkmcnt(0)
	v_perm_b32 v142, v131, v134, s22
	v_perm_b32 v138, v131, v134, s23
	v_perm_b32 v134, v132, v130, s22
	v_perm_b32 v130, v132, v130, s23
	s_waitcnt lgkmcnt(5)
	v_perm_b32 v131, v137, v136, s20
	v_perm_b32 v132, v137, v136, s21
	s_waitcnt lgkmcnt(4)
	v_perm_b32 v133, v141, v140, s20
	v_perm_b32 v136, v141, v140, s21
	v_perm_b32 v143, v133, v131, s22
	v_perm_b32 v139, v133, v131, s23
	v_perm_b32 v135, v136, v132, s22
	v_perm_b32 v131, v136, v132, s23
	s_waitcnt lgkmcnt(3)
	v_perm_b32 v132, v145, v144, s20
	v_perm_b32 v133, v145, v144, s21
	s_waitcnt lgkmcnt(2)
	v_perm_b32 v136, v157, v156, s20
	v_perm_b32 v137, v157, v156, s21
	v_perm_b32 v144, v136, v132, s22
	v_perm_b32 v140, v136, v132, s23
	v_perm_b32 v136, v137, v133, s22
	v_perm_b32 v132, v137, v133, s23
	s_waitcnt lgkmcnt(1)
	v_perm_b32 v133, v159, v158, s20
	v_perm_b32 v150, v159, v158, s21
	s_waitcnt lgkmcnt(0)
	v_perm_b32 v137, v161, v160, s20
	v_perm_b32 v156, v161, v160, s21
	v_perm_b32 v145, v137, v133, s22
	v_perm_b32 v141, v137, v133, s23
	v_perm_b32 v137, v156, v150, s22
	v_perm_b32 v133, v156, v150, s23
.LBB0_203:
	s_ashr_i32 s0, s30, 31
	v_add_u32_e32 v156, s31, v148
	s_add_u32 s8, s8, s30
	s_addc_u32 s9, s9, s0
	v_ashrrev_i32_e32 v157, 31, v156
	v_lshl_add_u64 v[158:159], s[8:9], 0, v[146:147]
	v_lshlrev_b64 v[156:157], 11, v[156:157]
	v_lshl_add_u64 v[156:157], v[158:159], 0, v[156:157]
	global_store_dwordx4 v[156:157], v[142:145], off nt
	global_store_dwordx4 v[156:157], v[138:141], off offset:2048 nt
	s_nop 1
	v_add_co_u32_e32 v138, vcc, 0x1000, v156
	s_nop 1
	v_addc_co_u32_e32 v139, vcc, 0, v157, vcc
	s_andn2_b64 vcc, exec, s[6:7]
	global_store_dwordx4 v[138:139], v[134:137], off nt
	global_store_dwordx4 v[138:139], v[130:133], off offset:2048 nt
	s_cbranch_vccnz .LBB0_209
	s_or_b32 s12, s28, 1
	s_cmp_gt_i32 s12, 0xffff
	s_mov_b64 s[10:11], -1
	s_cbranch_scc0 .LBB0_206
	s_add_i32 s0, s28, 0xffff0001
	s_lshl_b32 s6, s28, 1
	s_lshr_b32 s0, s0, 10
	s_and_b32 s7, s6, 0x780
	s_lshl_b32 s6, s12, 5
	s_and_b32 s6, s6, 0x7e0
	s_lshl_b64 s[8:9], s[0:1], 24
	s_add_u32 s8, s86, s8
	s_addc_u32 s9, s87, s9
	s_mov_b64 s[10:11], 0

; #define FP8_ITEM_LOAD(rv, W, N, k0, n0) do { const float* wsrc_ = (W) + (size_t)((k0) + (lane >> 3)) * (N) + (n0) + 4 * (lane & 7); \
;         _Pragma("unroll") for (int i_ = 0; i_ < 16; ++i_) rv[i_] = __builtin_nontemporal_load((const f32x4*)(wsrc_ + (size_t)(8 * i_) * (N))); } while (0)
; __device__ __forceinline__ void conv_dyn(Frame& F, const Args& a, int limit) {
;     ...
;         if (nid < CONV_NCHUNK) { const ConvItem c = conv_decode(a, n0 + 1); FP8_ITEM_LOAD(rb, c.W, c.NN, c.k0, c.n0); }
;         if (F.tid == 0) slot[2 + par] = claim;
;         asm volatile("s_waitcnt lgkmcnt(0)\n\ts_barrier" ::: "memory");
;         id = nid; nid = slot[2 + par]; par ^= 1;
.LBB0_208:
	s_waitcnt vmcnt(23)
	v_or_b32_e32 v66, s7, v1
	v_mul_hi_i32_i24_e32 v67, s10, v66
	v_mul_i32_i24_e32 v66, s10, v66
	v_lshl_add_u64 v[66:67], v[66:67], 2, s[8:9]
	s_ashr_i32 s7, s6, 31
	v_lshl_add_u64 v[66:67], s[6:7], 2, v[66:67]
	v_lshlrev_b32_e32 v150, 2, v148
	v_lshl_add_u64 v[66:67], v[66:67], 0, v[150:151]
	s_lshl_b32 s0, s10, 5
	s_waitcnt vmcnt(21)
	v_lshl_add_u64 v[74:75], v[66:67], 0, s[0:1]
	global_load_dwordx4 v[66:69], v[66:67], off nt
	s_nop 0
	global_load_dwordx4 v[70:73], v[74:75], off nt
	v_lshl_add_u64 v[74:75], v[74:75], 0, s[0:1]
	s_waitcnt vmcnt(21)
	v_lshl_add_u64 v[82:83], v[74:75], 0, s[0:1]
	global_load_dwordx4 v[74:77], v[74:75], off nt
	s_nop 0
	global_load_dwordx4 v[78:81], v[82:83], off nt
	v_lshl_add_u64 v[82:83], v[82:83], 0, s[0:1]
	s_waitcnt vmcnt(21)
	v_lshl_add_u64 v[90:91], v[82:83], 0, s[0:1]
	global_load_dwordx4 v[82:85], v[82:83], off nt
	s_nop 0
	global_load_dwordx4 v[86:89], v[90:91], off nt
	v_lshl_add_u64 v[90:91], v[90:91], 0, s[0:1]
	s_waitcnt vmcnt(21)
	v_lshl_add_u64 v[98:99], v[90:91], 0, s[0:1]
	s_waitcnt vmcnt(20)
	v_lshl_add_u64 v[102:103], v[98:99], 0, s[0:1]
	s_waitcnt vmcnt(19)
	v_lshl_add_u64 v[106:107], v[102:103], 0, s[0:1]
	s_waitcnt vmcnt(18)
	v_lshl_add_u64 v[110:111], v[106:107], 0, s[0:1]
	s_waitcnt vmcnt(17)
	v_lshl_add_u64 v[114:115], v[110:111], 0, s[0:1]
	s_waitcnt vmcnt(16)
	v_lshl_add_u64 v[118:119], v[114:115], 0, s[0:1]
	s_waitcnt vmcnt(15)
	v_lshl_add_u64 v[122:123], v[118:119], 0, s[0:1]
	s_waitcnt vmcnt(14)
	v_lshl_add_u64 v[126:127], v[122:123], 0, s[0:1]
	global_load_dwordx4 v[90:93], v[90:91], off nt
	s_nop 0
	global_load_dwordx4 v[94:97], v[98:99], off nt
	s_nop 0
	global_load_dwordx4 v[98:101], v[102:103], off nt
	s_nop 0
	global_load_dwordx4 v[102:105], v[106:107], off nt
	s_nop 0
	global_load_dwordx4 v[106:109], v[110:111], off nt
	s_nop 0
	global_load_dwordx4 v[110:113], v[114:115], off nt
	s_nop 0
	global_load_dwordx4 v[114:117], v[118:119], off nt
	s_nop 0
	global_load_dwordx4 v[118:121], v[122:123], off nt
	s_nop 0
	global_load_dwordx4 v[122:125], v[126:127], off nt
	v_lshl_add_u64 v[126:127], v[126:127], 0, s[0:1]
	global_load_dwordx4 v[126:129], v[126:127], off nt
.LBB0_209:
	s_and_saveexec_b64 s[6:7], s[2:3]
	s_cbranch_execz .LBB0_176
	s_lshl_b32 s0, s27, 2
	s_add_i32 s0, s0, 0
	s_add_i32 s0, s0, 0x21008
	v_mov_b32_e32 v130, s0
	ds_write_b32 v130, v155
	s_branch .LBB0_176

; __device__ __forceinline__ void conv_dyn(Frame& F, const Args& a, int limit) {
;     ...
;         int claim = CONV_NCHUNK;
;         if (F.tid == 0 && nid < limit) claim = (int)__hip_atomic_fetch_add(F.ctl + CW_CONV, 1u, RLX_AGENT);
.LBB0_257:
	s_cmpk_lt_i32 s14, 0x1800
	s_cselect_b64 s[8:9], -1, 0
	s_cmpk_gt_i32 s14, 0x17ff
	s_cselect_b64 s[6:7], -1, 0
	s_and_b64 s[10:11], s[2:3], s[8:9]
	v_mov_b32_e32 v155, 0x1800
	s_and_saveexec_b64 s[4:5], s[10:11]
	s_cbranch_execz .LBB0_261
	s_mov_b64 s[12:13], exec
	v_mbcnt_lo_u32_b32 v130, s12, 0
	v_mbcnt_hi_u32_b32 v130, s13, v130
	v_cmp_eq_u32_e32 vcc, 0, v130
	s_and_saveexec_b64 s[10:11], vcc
	s_cbranch_execz .LBB0_260
	s_bcnt1_i32_b64 s0, s[12:13]
	v_mov_b32_e32 v131, s0
	global_atomic_add v131, v151, v131, s[76:77] offset:512 sc0
.LBB0_260:
	s_or_b64 exec, exec, s[10:11]
	s_waitcnt vmcnt(0)
	v_readfirstlane_b32 s0, v131
	s_nop 1
	v_add_u32_e32 v155, s0, v130

; __device__ __forceinline__ unsigned f8x4u(float a, float b, float c, float d, float sc) {
;     int w = __builtin_amdgcn_cvt_pk_fp8_f32(a * sc, b * sc, 0, false); return (unsigned)__builtin_amdgcn_cvt_pk_fp8_f32(c * sc, d * sc, w, true);
; }
.LBB0_265:
	s_mov_b64 s[12:13], -1
	s_andn2_b64 vcc, exec, s[10:11]
	v_add_u32_e32 v161, 32, v152
	v_add_u32_e32 v160, 48, v152
	v_add_u32_e32 v159, 64, v152
	v_add_u32_e32 v158, 0x50, v152
	v_add_u32_e32 v157, 0x60, v152
	v_add_u32_e32 v156, 0x70, v152
	s_cbranch_vccnz .LBB0_267
	s_waitcnt vmcnt(19)
	v_mul_f32_e32 v130, s0, v2
	v_mul_f32_e32 v131, s0, v3
	v_mov_b32_e32 v132, v151
	v_cvt_pk_fp8_f32 v132, v130, v131
	s_waitcnt vmcnt(18)
	v_mul_f32_e32 v133, s0, v6
	v_mul_f32_e32 v134, s0, v7
	v_mov_b32_e32 v135, v151
	v_cvt_pk_fp8_f32 v135, v133, v134
	v_mul_f32_e32 v130, s0, v4
	v_mul_f32_e32 v131, s0, v5
	v_cvt_pk_fp8_f32 v132, v130, v131 op_sel:[0,0,1]
	v_mul_f32_e32 v130, s0, v8
	v_mul_f32_e32 v131, s0, v9
	v_cvt_pk_fp8_f32 v135, v130, v131 op_sel:[0,0,1]
	s_waitcnt vmcnt(17)
	v_mul_f32_e32 v130, s0, v10
	v_mul_f32_e32 v131, s0, v11
	v_mov_b32_e32 v133, v151
	v_cvt_pk_fp8_f32 v133, v130, v131
	s_waitcnt vmcnt(16)
	v_mul_f32_e32 v134, s0, v14
	v_mul_f32_e32 v136, s0, v15
	v_mov_b32_e32 v137, v151
	v_cvt_pk_fp8_f32 v137, v134, v136
	v_mul_f32_e32 v130, s0, v12
	v_mul_f32_e32 v131, s0, v13
	v_cvt_pk_fp8_f32 v133, v130, v131 op_sel:[0,0,1]
	v_mul_f32_e32 v130, s0, v16
	v_mul_f32_e32 v131, s0, v17
	v_cvt_pk_fp8_f32 v137, v130, v131 op_sel:[0,0,1]
	s_waitcnt vmcnt(15)
	v_mul_f32_e32 v130, s0, v18
	v_mul_f32_e32 v131, s0, v19
	v_mov_b32_e32 v134, v151
	v_cvt_pk_fp8_f32 v134, v130, v131
	s_waitcnt vmcnt(14)
	v_mul_f32_e32 v136, s0, v22
	v_mul_f32_e32 v138, s0, v23
	v_mov_b32_e32 v139, v151
	v_cvt_pk_fp8_f32 v139, v136, v138
	v_mul_f32_e32 v130, s0, v20
	v_mul_f32_e32 v131, s0, v21
	v_cvt_pk_fp8_f32 v134, v130, v131 op_sel:[0,0,1]
	v_mul_f32_e32 v130, s0, v24
	v_mul_f32_e32 v131, s0, v25
	v_cvt_pk_fp8_f32 v139, v130, v131 op_sel:[0,0,1]
	s_waitcnt vmcnt(13)
	v_mul_f32_e32 v130, s0, v26
	v_mul_f32_e32 v131, s0, v27
	v_mov_b32_e32 v136, v151
	v_cvt_pk_fp8_f32 v136, v130, v131
	s_waitcnt vmcnt(12)
	v_mul_f32_e32 v138, s0, v30
	v_mul_f32_e32 v140, s0, v31
	v_mov_b32_e32 v141, v151
	v_cvt_pk_fp8_f32 v141, v138, v140
	v_mul_f32_e32 v130, s0, v28
	v_mul_f32_e32 v131, s0, v29
	v_cvt_pk_fp8_f32 v136, v130, v131 op_sel:[0,0,1]
	v_mul_f32_e32 v130, s0, v32
	v_mul_f32_e32 v131, s0, v33
	v_cvt_pk_fp8_f32 v141, v130, v131 op_sel:[0,0,1]
	ds_write2st64_b32 v152, v132, v135 offset1:1
	ds_write2_b32 v152, v133, v137 offset0:132 offset1:196
	ds_write2st64_b32 v161, v134, v139 offset0:4 offset1:5
	ds_write2st64_b32 v160, v136, v141 offset0:6 offset1:7
	s_waitcnt vmcnt(11)
	v_mul_f32_e32 v130, s0, v34
	v_mul_f32_e32 v131, s0, v35
	v_mov_b32_e32 v132, v151
	v_cvt_pk_fp8_f32 v132, v130, v131
	s_waitcnt vmcnt(10)
	v_mul_f32_e32 v133, s0, v38
	v_mul_f32_e32 v134, s0, v39
	v_mov_b32_e32 v135, v151
	v_cvt_pk_fp8_f32 v135, v133, v134
	v_mul_f32_e32 v130, s0, v36
	v_mul_f32_e32 v131, s0, v37
	v_cvt_pk_fp8_f32 v132, v130, v131 op_sel:[0,0,1]
	v_mul_f32_e32 v130, s0, v40
	v_mul_f32_e32 v131, s0, v41
	v_cvt_pk_fp8_f32 v135, v130, v131 op_sel:[0,0,1]
	s_waitcnt vmcnt(9)
	v_mul_f32_e32 v130, s0, v42
	v_mul_f32_e32 v131, s0, v43
	v_mov_b32_e32 v133, v151
	v_cvt_pk_fp8_f32 v133, v130, v131
	s_waitcnt vmcnt(8)
	v_mul_f32_e32 v134, s0, v46
	v_mul_f32_e32 v136, s0, v47
	v_mov_b32_e32 v137, v151
	v_cvt_pk_fp8_f32 v137, v134, v136
	v_mul_f32_e32 v130, s0, v44
	v_mul_f32_e32 v131, s0, v45
	v_cvt_pk_fp8_f32 v133, v130, v131 op_sel:[0,0,1]
	v_mul_f32_e32 v130, s0, v48
	v_mul_f32_e32 v131, s0, v49
	v_cvt_pk_fp8_f32 v137, v130, v131 op_sel:[0,0,1]
	s_waitcnt vmcnt(7)
	v_mul_f32_e32 v130, s0, v50
	v_mul_f32_e32 v131, s0, v51
	v_mov_b32_e32 v134, v151
	v_cvt_pk_fp8_f32 v134, v130, v131
	s_waitcnt vmcnt(6)
	v_mul_f32_e32 v136, s0, v54
	v_mul_f32_e32 v138, s0, v55
	v_mov_b32_e32 v139, v151
	v_cvt_pk_fp8_f32 v139, v136, v138
	v_mul_f32_e32 v130, s0, v52
	v_mul_f32_e32 v131, s0, v53
	v_cvt_pk_fp8_f32 v134, v130, v131 op_sel:[0,0,1]
	v_mul_f32_e32 v130, s0, v56
	v_mul_f32_e32 v131, s0, v57
	v_cvt_pk_fp8_f32 v139, v130, v131 op_sel:[0,0,1]
	s_waitcnt vmcnt(5)
	v_mul_f32_e32 v130, s0, v58
	v_mul_f32_e32 v131, s0, v59
	v_mov_b32_e32 v136, v151
	v_cvt_pk_fp8_f32 v136, v130, v131
	s_waitcnt vmcnt(4)
	v_mul_f32_e32 v138, s0, v62
	v_mul_f32_e32 v140, s0, v63
	v_mov_b32_e32 v141, v151
	v_cvt_pk_fp8_f32 v141, v138, v140
	v_mul_f32_e32 v130, s0, v60
	v_mul_f32_e32 v131, s0, v61
	v_cvt_pk_fp8_f32 v136, v130, v131 op_sel:[0,0,1]
	v_mul_f32_e32 v130, s0, v64
	v_mul_f32_e32 v131, s0, v65
	v_cvt_pk_fp8_f32 v141, v130, v131 op_sel:[0,0,1]
	ds_write2st64_b32 v159, v132, v135 offset0:8 offset1:9
	ds_write2st64_b32 v158, v133, v137 offset0:10 offset1:11
	ds_write2st64_b32 v157, v134, v139 offset0:12 offset1:13
	ds_write2st64_b32 v156, v136, v141 offset0:14 offset1:15
	s_waitcnt lgkmcnt(0)
	ds_read2_b32 v[130:131], v149 offset1:8
	ds_read2_b32 v[132:133], v149 offset0:16 offset1:24
	ds_read2_b32 v[136:137], v149 offset0:32 offset1:40
	ds_read2_b32 v[140:141], v149 offset0:48 offset1:56
	ds_read2_b32 v[144:145], v149 offset0:64 offset1:72
	ds_read2_b32 v[162:163], v149 offset0:80 offset1:88
	ds_read2_b32 v[164:165], v149 offset0:96 offset1:104
	ds_read2_b32 v[166:167], v149 offset0:112 offset1:120
	s_waitcnt lgkmcnt(7)
	v_perm_b32 v134, v131, v130, s20
	v_perm_b32 v130, v131, v130, s21
	s_waitcnt lgkmcnt(6)
	v_perm_b32 v131, v133, v132, s20
	v_perm_b32 v132, v133, v132, s21
	s_waitcnt lgkmcnt(0)
	v_perm_b32 v142, v131, v134, s22
	v_perm_b32 v138, v131, v134, s23
	v_perm_b32 v134, v132, v130, s22
	v_perm_b32 v130, v132, v130, s23
	s_waitcnt lgkmcnt(5)
	v_perm_b32 v131, v137, v136, s20
	v_perm_b32 v132, v137, v136, s21
	s_waitcnt lgkmcnt(4)
	v_perm_b32 v133, v141, v140, s20
	v_perm_b32 v136, v141, v140, s21
	v_perm_b32 v143, v133, v131, s22
	v_perm_b32 v139, v133, v131, s23
	v_perm_b32 v135, v136, v132, s22
	v_perm_b32 v131, v136, v132, s23
	s_waitcnt lgkmcnt(3)
	v_perm_b32 v132, v145, v144, s20
	v_perm_b32 v133, v145, v144, s21
	s_waitcnt lgkmcnt(2)
	v_perm_b32 v136, v163, v162, s20
	v_perm_b32 v137, v163, v162, s21
	v_perm_b32 v144, v136, v132, s22
	v_perm_b32 v140, v136, v132, s23
	v_perm_b32 v136, v137, v133, s22
	v_perm_b32 v132, v137, v133, s23
	s_waitcnt lgkmcnt(1)
	v_perm_b32 v133, v165, v164, s20
	v_perm_b32 v150, v165, v164, s21
	s_waitcnt lgkmcnt(0)
	v_perm_b32 v137, v167, v166, s20
	v_perm_b32 v162, v167, v166, s21
	v_perm_b32 v145, v137, v133, s22
	v_perm_b32 v141, v137, v133, s23
	v_perm_b32 v137, v162, v150, s22
	v_perm_b32 v133, v162, v150, s23
	s_mov_b64 s[12:13], 0
; __device__ __forceinline__ unsigned q8x4(float a, float b, float c, float d, float sc) {
;     const float M = 12582912.0f;
;     const unsigned ua = __builtin_bit_cast(unsigned, __builtin_amdgcn_fmed3f(__builtin_fmaf(a, sc, M), M - 127.0f, M + 127.0f)), ub = __builtin_bit_cast(unsigned, __builtin_amdgcn_fmed3f(__builtin_fmaf(b, sc, M), M - 127.0f, M + 127.0f));
;     const unsigned uc = __builtin_bit_cast(unsigned, __builtin_amdgcn_fmed3f(__builtin_fmaf(c, sc, M), M - 127.0f, M + 127.0f)), ud = __builtin_bit_cast(unsigned, __builtin_amdgcn_fmed3f(__builtin_fmaf(d, sc, M), M - 127.0f, M + 127.0f));
;     return __builtin_amdgcn_perm(ub, ua, 0x0c0c0400u) | __builtin_amdgcn_perm(ud, uc, 0x04000c0cu);
.LBB0_267:
	s_andn2_b64 vcc, exec, s[12:13]
	s_cbranch_vccnz .LBB0_269
	s_waitcnt vmcnt(19)
	v_fma_f32 v130, s0, v2, v153
	v_fma_f32 v131, s0, v3, v153
	v_fma_f32 v132, s0, v4, v153
	v_fma_f32 v133, s0, v5, v153
	v_med3_f32 v130, v130, s24, v154
	v_med3_f32 v131, v131, s24, v154
	v_med3_f32 v132, v132, s24, v154
	v_med3_f32 v133, v133, s24, v154
	v_perm_b32 v130, v131, v130, s25
	v_perm_b32 v131, v133, v132, s26
	v_or_b32_e32 v130, v130, v131
	s_waitcnt vmcnt(18)
	v_fma_f32 v131, s0, v6, v153
	v_fma_f32 v132, s0, v7, v153
	v_fma_f32 v133, s0, v8, v153
	v_fma_f32 v134, s0, v9, v153
	v_med3_f32 v131, v131, s24, v154
	v_med3_f32 v132, v132, s24, v154
	v_med3_f32 v133, v133, s24, v154
	v_med3_f32 v134, v134, s24, v154
	v_perm_b32 v131, v132, v131, s25
	v_perm_b32 v132, v134, v133, s26
	v_or_b32_e32 v131, v131, v132
	ds_write2st64_b32 v152, v130, v131 offset1:1
	s_waitcnt vmcnt(17)
	v_fma_f32 v130, s0, v10, v153
	v_fma_f32 v131, s0, v11, v153
	v_fma_f32 v132, s0, v12, v153
	v_fma_f32 v133, s0, v13, v153
	v_med3_f32 v130, v130, s24, v154
	v_med3_f32 v131, v131, s24, v154
	v_med3_f32 v132, v132, s24, v154
	v_med3_f32 v133, v133, s24, v154
	v_perm_b32 v130, v131, v130, s25
	v_perm_b32 v131, v133, v132, s26
	v_or_b32_e32 v130, v130, v131
	s_waitcnt vmcnt(16)
	v_fma_f32 v131, s0, v14, v153
	v_fma_f32 v132, s0, v15, v153
	v_fma_f32 v133, s0, v16, v153
	v_fma_f32 v134, s0, v17, v153
	v_med3_f32 v131, v131, s24, v154
	v_med3_f32 v132, v132, s24, v154
	v_med3_f32 v133, v133, s24, v154
	v_med3_f32 v134, v134, s24, v154
	v_perm_b32 v131, v132, v131, s25
	v_perm_b32 v132, v134, v133, s26
	v_or_b32_e32 v131, v131, v132
	ds_write2_b32 v152, v130, v131 offset0:132 offset1:196
	s_waitcnt vmcnt(15)
	v_fma_f32 v130, s0, v18, v153
	v_fma_f32 v131, s0, v19, v153
	v_fma_f32 v132, s0, v20, v153
	v_fma_f32 v133, s0, v21, v153
	v_med3_f32 v130, v130, s24, v154
	v_med3_f32 v131, v131, s24, v154
	v_med3_f32 v132, v132, s24, v154
	v_med3_f32 v133, v133, s24, v154
	v_perm_b32 v130, v131, v130, s25
	v_perm_b32 v131, v133, v132, s26
	v_or_b32_e32 v130, v130, v131
	s_waitcnt vmcnt(14)
	v_fma_f32 v131, s0, v22, v153
	v_fma_f32 v132, s0, v23, v153
	v_fma_f32 v133, s0, v24, v153
	v_fma_f32 v134, s0, v25, v153
	v_med3_f32 v131, v131, s24, v154
	v_med3_f32 v132, v132, s24, v154
	v_med3_f32 v133, v133, s24, v154
	v_med3_f32 v134, v134, s24, v154
	v_perm_b32 v131, v132, v131, s25
	v_perm_b32 v132, v134, v133, s26
	v_or_b32_e32 v131, v131, v132
	ds_write2st64_b32 v161, v130, v131 offset0:4 offset1:5
	s_waitcnt vmcnt(13)
	v_fma_f32 v130, s0, v26, v153
	v_fma_f32 v131, s0, v27, v153
	v_fma_f32 v132, s0, v28, v153
	v_fma_f32 v133, s0, v29, v153
	v_med3_f32 v130, v130, s24, v154
	v_med3_f32 v131, v131, s24, v154
	v_med3_f32 v132, v132, s24, v154
	v_med3_f32 v133, v133, s24, v154
	v_perm_b32 v130, v131, v130, s25
	v_perm_b32 v131, v133, v132, s26
	v_or_b32_e32 v130, v130, v131
	s_waitcnt vmcnt(12)
	v_fma_f32 v131, s0, v30, v153
	v_fma_f32 v132, s0, v31, v153
	v_fma_f32 v133, s0, v32, v153
	v_fma_f32 v134, s0, v33, v153
	v_med3_f32 v131, v131, s24, v154
	v_med3_f32 v132, v132, s24, v154
	v_med3_f32 v133, v133, s24, v154
	v_med3_f32 v134, v134, s24, v154
	v_perm_b32 v131, v132, v131, s25
	v_perm_b32 v132, v134, v133, s26
	v_or_b32_e32 v131, v131, v132
	ds_write2st64_b32 v160, v130, v131 offset0:6 offset1:7
	s_waitcnt vmcnt(11)
	v_fma_f32 v130, s0, v34, v153
	v_fma_f32 v131, s0, v35, v153
	v_fma_f32 v132, s0, v36, v153
	v_fma_f32 v133, s0, v37, v153
	v_med3_f32 v130, v130, s24, v154
	v_med3_f32 v131, v131, s24, v154
	v_med3_f32 v132, v132, s24, v154
	v_med3_f32 v133, v133, s24, v154
	v_perm_b32 v130, v131, v130, s25
	v_perm_b32 v131, v133, v132, s26
	v_or_b32_e32 v130, v130, v131
	s_waitcnt vmcnt(10)
	v_fma_f32 v131, s0, v38, v153
	v_fma_f32 v132, s0, v39, v153
	v_fma_f32 v133, s0, v40, v153
	v_fma_f32 v134, s0, v41, v153
	v_med3_f32 v131, v131, s24, v154
	v_med3_f32 v132, v132, s24, v154
	v_med3_f32 v133, v133, s24, v154
	v_med3_f32 v134, v134, s24, v154
	v_perm_b32 v131, v132, v131, s25
	v_perm_b32 v132, v134, v133, s26
	v_or_b32_e32 v131, v131, v132
	ds_write2st64_b32 v159, v130, v131 offset0:8 offset1:9
	s_waitcnt vmcnt(9)
	v_fma_f32 v130, s0, v42, v153
	v_fma_f32 v131, s0, v43, v153
	v_fma_f32 v132, s0, v44, v153
	v_fma_f32 v133, s0, v45, v153
	v_med3_f32 v130, v130, s24, v154
	v_med3_f32 v131, v131, s24, v154
	v_med3_f32 v132, v132, s24, v154
	v_med3_f32 v133, v133, s24, v154
	v_perm_b32 v130, v131, v130, s25
	v_perm_b32 v131, v133, v132, s26
	v_or_b32_e32 v130, v130, v131
	s_waitcnt vmcnt(8)
; #define FP8_ITEM_LOAD(rv, W, N, k0, n0) do { const float* wsrc_ = (W) + (size_t)((k0) + (lane >> 3)) * (N) + (n0) + 4 * (lane & 7); \
;         _Pragma("unroll") for (int i_ = 0; i_ < 16; ++i_) rv[i_] = __builtin_nontemporal_load((const f32x4*)(wsrc_ + (size_t)(8 * i_) * (N))); } while (0)
; #define FP8_ITEM_STORE(rv, K, WT, k0, drow0, scale) W8_ITEM_STORE(f8x4u, rv, K, WT, k0, drow0, scale)
; #define I8_ITEM_STORE(rv, K, WT, k0, drow0, scale) W8_ITEM_STORE(q8x4, rv, K, WT, k0, drow0, scale)
; __device__ __forceinline__ void conv_dyn(Frame& F, const Args& a, int limit) {
;     ...
;         { const ConvItem c = conv_decode(a, r0); if (c.i8) I8_ITEM_STORE(ra, c.KK, c.WT, c.k0, c.d0, c.scale); else FP8_ITEM_STORE(ra, c.KK, c.WT, c.k0, c.d0, c.scale); }
;         if (nid < CONV_NCHUNK) { const ConvItem c = conv_decode(a, n0); FP8_ITEM_LOAD(ra, c.W, c.NN, c.k0, c.n0); }
	v_fma_f32 v131, s0, v46, v153
	v_fma_f32 v132, s0, v47, v153
	v_fma_f32 v133, s0, v48, v153
	v_fma_f32 v134, s0, v49, v153
	v_med3_f32 v131, v131, s24, v154
	v_med3_f32 v132, v132, s24, v154
	v_med3_f32 v133, v133, s24, v154
	v_med3_f32 v134, v134, s24, v154
	v_perm_b32 v131, v132, v131, s25
	v_perm_b32 v132, v134, v133, s26
	v_or_b32_e32 v131, v131, v132
	ds_write2st64_b32 v158, v130, v131 offset0:10 offset1:11
	s_waitcnt vmcnt(7)
	v_fma_f32 v130, s0, v50, v153
	v_fma_f32 v131, s0, v51, v153
	v_fma_f32 v132, s0, v52, v153
	v_fma_f32 v133, s0, v53, v153
	v_med3_f32 v130, v130, s24, v154
	v_med3_f32 v131, v131, s24, v154
	v_med3_f32 v132, v132, s24, v154
	v_med3_f32 v133, v133, s24, v154
	v_perm_b32 v130, v131, v130, s25
	v_perm_b32 v131, v133, v132, s26
	v_or_b32_e32 v130, v130, v131
	s_waitcnt vmcnt(6)
	v_fma_f32 v131, s0, v54, v153
	v_fma_f32 v132, s0, v55, v153
	v_fma_f32 v133, s0, v56, v153
	v_fma_f32 v134, s0, v57, v153
	v_med3_f32 v131, v131, s24, v154
	v_med3_f32 v132, v132, s24, v154
	v_med3_f32 v133, v133, s24, v154
	v_med3_f32 v134, v134, s24, v154
	v_perm_b32 v131, v132, v131, s25
	v_perm_b32 v132, v134, v133, s26
	v_or_b32_e32 v131, v131, v132
	ds_write2st64_b32 v157, v130, v131 offset0:12 offset1:13
	s_waitcnt vmcnt(5)
	v_fma_f32 v130, s0, v58, v153
	v_fma_f32 v131, s0, v59, v153
	v_fma_f32 v132, s0, v60, v153
	v_fma_f32 v133, s0, v61, v153
	v_med3_f32 v130, v130, s24, v154
	v_med3_f32 v131, v131, s24, v154
	v_med3_f32 v132, v132, s24, v154
	v_med3_f32 v133, v133, s24, v154
	v_perm_b32 v130, v131, v130, s25
	v_perm_b32 v131, v133, v132, s26
	v_or_b32_e32 v130, v130, v131
	s_waitcnt vmcnt(4)
	v_fma_f32 v131, s0, v62, v153
	v_fma_f32 v132, s0, v63, v153
	v_fma_f32 v133, s0, v64, v153
	v_fma_f32 v134, s0, v65, v153
	v_med3_f32 v131, v131, s24, v154
	v_med3_f32 v132, v132, s24, v154
	v_med3_f32 v133, v133, s24, v154
	v_med3_f32 v134, v134, s24, v154
	v_perm_b32 v131, v132, v131, s25
	v_perm_b32 v132, v134, v133, s26
	v_or_b32_e32 v131, v131, v132
	ds_write2st64_b32 v156, v130, v131 offset0:14 offset1:15
	s_waitcnt lgkmcnt(0)
	ds_read2_b32 v[130:131], v149 offset1:8
	ds_read2_b32 v[132:133], v149 offset0:16 offset1:24
	ds_read2_b32 v[136:137], v149 offset0:32 offset1:40
	ds_read2_b32 v[140:141], v149 offset0:48 offset1:56
	ds_read2_b32 v[144:145], v149 offset0:64 offset1:72
	ds_read2_b32 v[162:163], v149 offset0:80 offset1:88
	ds_read2_b32 v[164:165], v149 offset0:96 offset1:104
	ds_read2_b32 v[166:167], v149 offset0:112 offset1:120
	s_waitcnt lgkmcnt(7)
	v_perm_b32 v134, v131, v130, s20
	v_perm_b32 v130, v131, v130, s21
	s_waitcnt lgkmcnt(6)
	v_perm_b32 v131, v133, v132, s20
	v_perm_b32 v132, v133, v132, s21
	s_waitcnt lgkmcnt(0)
	v_perm_b32 v142, v131, v134, s22
	v_perm_b32 v138, v131, v134, s23
	v_perm_b32 v134, v132, v130, s22
	v_perm_b32 v130, v132, v130, s23
	s_waitcnt lgkmcnt(5)
	v_perm_b32 v131, v137, v136, s20
	v_perm_b32 v132, v137, v136, s21
	s_waitcnt lgkmcnt(4)
	v_perm_b32 v133, v141, v140, s20
	v_perm_b32 v136, v141, v140, s21
	v_perm_b32 v143, v133, v131, s22
	v_perm_b32 v139, v133, v131, s23
	v_perm_b32 v135, v136, v132, s22
	v_perm_b32 v131, v136, v132, s23
	s_waitcnt lgkmcnt(3)
	v_perm_b32 v132, v145, v144, s20
	v_perm_b32 v133, v145, v144, s21
	s_waitcnt lgkmcnt(2)
	v_perm_b32 v136, v163, v162, s20
	v_perm_b32 v137, v163, v162, s21
	v_perm_b32 v144, v136, v132, s22
	v_perm_b32 v140, v136, v132, s23
	v_perm_b32 v136, v137, v133, s22
	v_perm_b32 v132, v137, v133, s23
	s_waitcnt lgkmcnt(1)
	v_perm_b32 v133, v165, v164, s20
	v_perm_b32 v150, v165, v164, s21
	s_waitcnt lgkmcnt(0)
	v_perm_b32 v137, v167, v166, s20
	v_perm_b32 v162, v167, v166, s21
	v_perm_b32 v145, v137, v133, s22
	v_perm_b32 v141, v137, v133, s23
	v_perm_b32 v137, v162, v150, s22
	v_perm_b32 v133, v162, v150, s23
.LBB0_269:
	s_lshl_b32 s28, s14, 4
	s_add_i32 s28, s28, s15
	s_ashr_i32 s0, s30, 31
	v_add_u32_e32 v162, s31, v148
	s_add_u32 s4, s4, s30
	s_addc_u32 s5, s5, s0
	v_ashrrev_i32_e32 v163, 31, v162
	v_lshl_add_u64 v[164:165], s[4:5], 0, v[146:147]
	v_lshlrev_b64 v[162:163], 11, v[162:163]
	v_lshl_add_u64 v[162:163], v[164:165], 0, v[162:163]
	global_store_dwordx4 v[162:163], v[142:145], off nt
	global_store_dwordx4 v[162:163], v[138:141], off offset:2048 nt
	s_nop 1
	v_add_co_u32_e32 v138, vcc, 0x1000, v162
	s_nop 1
	v_addc_co_u32_e32 v139, vcc, 0, v163, vcc
	global_store_dwordx4 v[138:139], v[134:137], off nt
	s_andn2_b64 vcc, exec, s[8:9]
	global_store_dwordx4 v[138:139], v[130:133], off offset:2048 nt
	v_cndmask_b32_e64 v134, 0, 1, s[8:9]
	v_cmp_ne_u32_e64 s[4:5], 1, v134
	s_cbranch_vccnz .LBB0_275
	s_cmp_gt_i32 s28, 0xffff
	s_mov_b64 s[12:13], -1
	s_cbranch_scc0 .LBB0_272
	s_add_i32 s0, s28, 0xffff0000
	s_lshl_b32 s8, s28, 1
	s_lshr_b32 s0, s0, 10
	s_and_b32 s9, s8, 0x780
	s_lshl_b32 s8, s28, 5
	s_and_b32 s8, s8, 0x7c0
	s_lshl_b64 s[10:11], s[0:1], 24
	s_add_u32 s10, s86, s10
	s_addc_u32 s11, s87, s11
	s_mov_b64 s[12:13], 0

; __device__ __forceinline__ ConvItem conv_decode(const Args& a, int r) {
;     ConvItem c;
;     if (r < CONV_I_GU) { constexpr int PER = (D / 128) * (2 * DFF / 32), NB = 2 * DFF / 32; const int e = r / PER, q = r % PER; c.KK = D; c.NN = 2 * DFF; c.k0 = 128 * (q / NB); c.n0 = 32 * (q % NB); c.d0 = map_wgu(c.n0);
;         c.W = a.wgu + (size_t)e * D * 2 * DFF; c.WT = a.ws + WS_WGU + (size_t)e * 2 * DFF * D; c.scale = SC_WGU; c.i8 = true; }
;     else { r -= CONV_I_GU; constexpr int PER = (DFF / 128) * (D / 32), NB = D / 32; const int e = r / PER, q = r % PER; c.KK = DFF; c.NN = D; c.k0 = 128 * (q / NB); c.n0 = 32 * (q % NB); c.d0 = c.n0;
;         c.W = a.wd + (size_t)e * DFF * D; c.WT = a.ws + WS_WD + (size_t)e * D * DFF; c.scale = SC_WD; c.i8 = false; }
.LBB0_283:
	s_ashr_i32 s0, s30, 31
	v_add_u32_e32 v156, s31, v148
	s_add_u32 s8, s8, s30
	s_addc_u32 s9, s9, s0
	v_ashrrev_i32_e32 v157, 31, v156
	v_lshl_add_u64 v[158:159], s[8:9], 0, v[146:147]
	v_lshlrev_b64 v[156:157], 11, v[156:157]
	v_lshl_add_u64 v[156:157], v[158:159], 0, v[156:157]
	global_store_dwordx4 v[156:157], v[142:145], off nt
	global_store_dwordx4 v[156:157], v[138:141], off offset:2048 nt
	s_nop 1
	v_add_co_u32_e32 v138, vcc, 0x1000, v156
	s_nop 1
	v_addc_co_u32_e32 v139, vcc, 0, v157, vcc
	s_and_b64 vcc, exec, s[4:5]
	global_store_dwordx4 v[138:139], v[134:137], off nt
	global_store_dwordx4 v[138:139], v[130:133], off offset:2048 nt
	s_cbranch_vccnz .LBB0_289
	s_or_b32 s12, s28, 1
	s_cmp_gt_i32 s12, 0xffff
	s_mov_b64 s[10:11], -1
	s_cbranch_scc0 .LBB0_286
	s_add_i32 s0, s28, 0xffff0001
	s_lshl_b32 s4, s28, 1
	s_lshr_b32 s0, s0, 10
	s_and_b32 s5, s4, 0x780
	s_lshl_b32 s4, s12, 5
	s_and_b32 s4, s4, 0x7e0
	s_lshl_b64 s[8:9], s[0:1], 24
	s_add_u32 s8, s86, s8
	s_addc_u32 s9, s87, s9
	s_mov_b64 s[10:11], 0

; #define FP8_ITEM_LOAD(rv, W, N, k0, n0) do { const float* wsrc_ = (W) + (size_t)((k0) + (lane >> 3)) * (N) + (n0) + 4 * (lane & 7); \
;         _Pragma("unroll") for (int i_ = 0; i_ < 16; ++i_) rv[i_] = __builtin_nontemporal_load((const f32x4*)(wsrc_ + (size_t)(8 * i_) * (N))); } while (0)
; __device__ __forceinline__ void conv_dyn(Frame& F, const Args& a, int limit) {
;     ...
;         if (nid < CONV_NCHUNK) { const ConvItem c = conv_decode(a, n0 + 1); FP8_ITEM_LOAD(rb, c.W, c.NN, c.k0, c.n0); }
;         if (F.tid == 0) slot[2 + par] = claim;
;         asm volatile("s_waitcnt lgkmcnt(0)\n\ts_barrier" ::: "memory");
;         id = nid; nid = slot[2 + par]; par ^= 1;
.LBB0_288:
	s_waitcnt vmcnt(23)
	v_or_b32_e32 v66, s5, v1
	v_mul_hi_i32_i24_e32 v67, s10, v66
	v_mul_i32_i24_e32 v66, s10, v66
	v_lshl_add_u64 v[66:67], v[66:67], 2, s[8:9]
	s_ashr_i32 s5, s4, 31
	v_lshl_add_u64 v[66:67], s[4:5], 2, v[66:67]
	v_lshlrev_b32_e32 v150, 2, v148
	v_lshl_add_u64 v[66:67], v[66:67], 0, v[150:151]
	s_lshl_b32 s0, s10, 5
	s_waitcnt vmcnt(21)
	v_lshl_add_u64 v[74:75], v[66:67], 0, s[0:1]
	global_load_dwordx4 v[66:69], v[66:67], off nt
	s_nop 0
	global_load_dwordx4 v[70:73], v[74:75], off nt
	v_lshl_add_u64 v[74:75], v[74:75], 0, s[0:1]
	s_waitcnt vmcnt(21)
	v_lshl_add_u64 v[82:83], v[74:75], 0, s[0:1]
	global_load_dwordx4 v[74:77], v[74:75], off nt
	s_nop 0
	global_load_dwordx4 v[78:81], v[82:83], off nt
	v_lshl_add_u64 v[82:83], v[82:83], 0, s[0:1]
	s_waitcnt vmcnt(21)
	v_lshl_add_u64 v[90:91], v[82:83], 0, s[0:1]
	global_load_dwordx4 v[82:85], v[82:83], off nt
	s_nop 0
	global_load_dwordx4 v[86:89], v[90:91], off nt
	v_lshl_add_u64 v[90:91], v[90:91], 0, s[0:1]
	s_waitcnt vmcnt(21)
	v_lshl_add_u64 v[98:99], v[90:91], 0, s[0:1]
	s_waitcnt vmcnt(20)
	v_lshl_add_u64 v[102:103], v[98:99], 0, s[0:1]
	s_waitcnt vmcnt(19)
	v_lshl_add_u64 v[106:107], v[102:103], 0, s[0:1]
	s_waitcnt vmcnt(18)
	v_lshl_add_u64 v[110:111], v[106:107], 0, s[0:1]
	s_waitcnt vmcnt(17)
	v_lshl_add_u64 v[114:115], v[110:111], 0, s[0:1]
	s_waitcnt vmcnt(16)
	v_lshl_add_u64 v[118:119], v[114:115], 0, s[0:1]
	s_waitcnt vmcnt(15)
	v_lshl_add_u64 v[122:123], v[118:119], 0, s[0:1]
	s_waitcnt vmcnt(14)
	v_lshl_add_u64 v[126:127], v[122:123], 0, s[0:1]
	global_load_dwordx4 v[90:93], v[90:91], off nt
	s_nop 0
	global_load_dwordx4 v[94:97], v[98:99], off nt
	s_nop 0
	global_load_dwordx4 v[98:101], v[102:103], off nt
	s_nop 0
	global_load_dwordx4 v[102:105], v[106:107], off nt
	s_nop 0
	global_load_dwordx4 v[106:109], v[110:111], off nt
	s_nop 0
	global_load_dwordx4 v[110:113], v[114:115], off nt
	s_nop 0
	global_load_dwordx4 v[114:117], v[118:119], off nt
	s_nop 0
	global_load_dwordx4 v[118:121], v[122:123], off nt
	s_nop 0
	global_load_dwordx4 v[122:125], v[126:127], off nt
	v_lshl_add_u64 v[126:127], v[126:127], 0, s[0:1]
	global_load_dwordx4 v[126:129], v[126:127], off nt
.LBB0_289:
	s_and_saveexec_b64 s[4:5], s[2:3]
	s_cbranch_execz .LBB0_256
	s_lshl_b32 s0, s27, 2
	s_add_i32 s0, s0, 0
	s_add_i32 s0, s0, 0x21008
	v_mov_b32_e32 v130, s0
	ds_write_b32 v130, v155
	s_branch .LBB0_256

; #define LAS __attribute__((address_space(3)))
; __device__ __forceinline__ void phase3_attn(Frame& F, const Args& a) {
;     ...
;         f32x4 st[10];
; #pragma unroll
;         for (int i = 0; i < 10; ++i) {
;             st[i] = (f32x4){0.f, 0.f, 0.f, 0.f};
; #pragma unroll
;             for (int s = 0; s < 4; ++s) {
;                 const bf16x8_t kf = *(const LAS bf16x8_t*)(F.lds + ATT_K_OFF + ((kt0 + i) * 16 + fr) * 256 + (((4 * s + fq) ^ fr) << 4));
;                 st[i] = __builtin_amdgcn_mfma_f32_16x16x32_bf16(kf, qf[s], st[i], 0, 0, 0);
;             }
;         }
.LBB0_414:
	s_barrier
	v_add_u32_e32 v10, v99, v88
	ds_read_b128 v[120:123], v10
	v_add_u32_e32 v11, v99, v89
	ds_read_b128 v[124:127], v11
	v_add_u32_e32 v12, v99, v90
	ds_read_b128 v[128:131], v12
	v_add_u32_e32 v13, v99, v91
	ds_read_b128 v[132:135], v13
	v_add_u32_e32 v116, v100, v88
	ds_read_b128 v[136:139], v116
	v_add_u32_e32 v117, v100, v89
	ds_read_b128 v[140:143], v117
	v_add_u32_e32 v118, v100, v90
	ds_read_b128 v[144:147], v118
	v_add_u32_e32 v119, v100, v91
	ds_read_b128 v[148:151], v119
	ds_read_b128 v[152:155], v10 offset:8192
	ds_read_b128 v[156:159], v11 offset:8192
	ds_read_b128 v[160:163], v12 offset:8192
	ds_read_b128 v[164:167], v13 offset:8192
	s_cmp_lg_u32 s31, 18
	s_cselect_b32 s1, s31, 17
	s_waitcnt lgkmcnt(11)
	v_mfma_f32_16x16x32_bf16 v[2:5], v[120:123], v[66:69], 0
	ds_read_b128 v[120:123], v10 offset:12288
	s_mul_hi_u32 s20, s1, 0xaaaaaaab
	s_lshr_b32 s20, s20, 1
	s_waitcnt lgkmcnt(11)
	v_mfma_f32_16x16x32_bf16 v[2:5], v[124:127], v[62:65], v[2:5]
	ds_read_b128 v[124:127], v11 offset:12288
	s_lshl_b32 s21, s20, 3
	s_add_i32 s21, s21, s28
	s_waitcnt lgkmcnt(11)
	v_mfma_f32_16x16x32_bf16 v[2:5], v[128:131], v[58:61], v[2:5]
	ds_read_b128 v[128:131], v12 offset:12288
	s_mul_i32 s50, s20, -3
	s_add_i32 s50, s50, s1
	s_waitcnt lgkmcnt(11)
	v_mfma_f32_16x16x32_bf16 v[42:45], v[132:135], v[54:57], v[2:5]
	ds_read_b128 v[132:135], v13 offset:12288
	s_mul_hi_i32 s1, s21, 0x2aaaaaab
	s_lshr_b32 s20, s1, 31
	s_waitcnt lgkmcnt(11)
	v_mfma_f32_16x16x32_bf16 v[6:9], v[136:139], v[66:69], 0
	ds_read_b128 v[136:139], v10 offset:16384
	s_ashr_i32 s51, s1, 1
	s_lshl_b32 s1, s50, 1
	s_waitcnt lgkmcnt(11)
	v_mfma_f32_16x16x32_bf16 v[6:9], v[140:143], v[62:65], v[6:9]
	ds_read_b128 v[140:143], v11 offset:16384
	s_add_i32 s51, s51, s20
	s_sub_i32 s20, 5, s1
	s_waitcnt lgkmcnt(11)
	v_mfma_f32_16x16x32_bf16 v[6:9], v[144:147], v[58:61], v[6:9]
	ds_read_b128 v[144:147], v12 offset:16384
	s_mul_i32 s52, s51, -12
	s_lshr_b32 s23, s29, s20
	s_waitcnt lgkmcnt(11)
	v_mfma_f32_16x16x32_bf16 v[46:49], v[148:151], v[54:57], v[6:9]
	ds_read_b128 v[148:151], v13 offset:16384
	s_lshl_b32 s20, -1, s20
	s_add_i32 s52, s52, s21
	s_waitcnt lgkmcnt(11)
	v_mfma_f32_16x16x32_bf16 v[2:5], v[152:155], v[66:69], 0
	ds_read_b128 v[152:155], v10 offset:20480
	s_andn2_b32 s53, s29, s20
	s_mul_i32 s95, s51, 0xc00000
	s_waitcnt lgkmcnt(11)
	v_mfma_f32_16x16x32_bf16 v[2:5], v[156:159], v[62:65], v[2:5]
	ds_read_b128 v[156:159], v11 offset:20480
	s_mul_hi_i32 s89, s51, 0xc00000
	s_add_u32 s54, s24, s95
	s_waitcnt lgkmcnt(11)
	v_mfma_f32_16x16x32_bf16 v[2:5], v[160:163], v[58:61], v[2:5]
	ds_read_b128 v[160:163], v12 offset:20480
	s_addc_u32 s55, s25, s89
	s_lshl_b32 s20, s52, 7
	s_waitcnt lgkmcnt(11)
	v_mfma_f32_16x16x32_bf16 v[38:41], v[164:167], v[54:57], v[2:5]
	ds_read_b128 v[164:167], v13 offset:20480
	s_ashr_i32 s21, s20, 31
	s_lshl_b64 s[20:21], s[20:21], 1
	s_waitcnt lgkmcnt(11)
	v_mfma_f32_16x16x32_bf16 v[6:9], v[120:123], v[66:69], 0
	ds_read_b128 v[120:123], v10 offset:24576
	s_add_u32 s56, s54, s20
	s_addc_u32 s55, s55, s21
	s_waitcnt lgkmcnt(11)
	v_mfma_f32_16x16x32_bf16 v[6:9], v[124:127], v[62:65], v[6:9]
	ds_read_b128 v[124:127], v11 offset:24576
	s_mul_i32 s54, s23, 0xc00
	s_add_u32 s80, s56, s54
	s_waitcnt lgkmcnt(11)
	v_mfma_f32_16x16x32_bf16 v[6:9], v[128:131], v[58:61], v[6:9]
	ds_read_b128 v[128:131], v12 offset:24576
	s_addc_u32 s81, s55, 0
	s_lshl_b32 s96, s53, 7
	s_waitcnt lgkmcnt(11)
	v_mfma_f32_16x16x32_bf16 v[34:37], v[132:135], v[54:57], v[6:9]
	ds_read_b128 v[132:135], v13 offset:24576
	s_add_i32 s55, s96, 0xffffff80
	s_cmp_eq_u32 s53, 0
	s_waitcnt lgkmcnt(11)
	v_mfma_f32_16x16x32_bf16 v[2:5], v[136:139], v[66:69], 0
	ds_read_b128 v[136:139], v10 offset:28672
	s_cselect_b32 s56, 0, s55
	s_cselect_b32 s60, 0x80, 0
	s_waitcnt lgkmcnt(11)
	v_mfma_f32_16x16x32_bf16 v[2:5], v[140:143], v[62:65], v[2:5]
	ds_read_b128 v[140:143], v11 offset:28672
	s_ashr_i32 s57, s56, 31
	s_lshl_b64 s[56:57], s[56:57], s1
	s_waitcnt lgkmcnt(11)
	v_mfma_f32_16x16x32_bf16 v[2:5], v[144:147], v[58:61], v[2:5]
	ds_read_b128 v[144:147], v12 offset:28672
	s_mul_hi_u32 s55, s56, 0xc00
	s_mulk_i32 s57, 0xc00
	s_waitcnt lgkmcnt(11)
	v_mfma_f32_16x16x32_bf16 v[30:33], v[148:151], v[54:57], v[2:5]
	ds_read_b128 v[148:151], v13 offset:28672
	s_add_i32 s55, s55, s57
	s_mulk_i32 s56, 0xc00
	s_waitcnt lgkmcnt(11)
	v_mfma_f32_16x16x32_bf16 v[6:9], v[152:155], v[66:69], 0
	ds_read_b128 v[152:155], v10 offset:32768
	s_add_u32 s58, s80, s56
	s_addc_u32 s59, s81, s55
	s_waitcnt lgkmcnt(11)
	v_mfma_f32_16x16x32_bf16 v[6:9], v[156:159], v[62:65], v[6:9]
	ds_read_b128 v[156:159], v11 offset:32768
	s_add_i32 s64, s60, s96
	s_waitcnt lgkmcnt(11)
	v_mfma_f32_16x16x32_bf16 v[6:9], v[160:163], v[58:61], v[6:9]
	ds_read_b128 v[160:163], v12 offset:32768
	s_waitcnt lgkmcnt(11)
	v_mfma_f32_16x16x32_bf16 v[26:29], v[164:167], v[54:57], v[6:9]
	ds_read_b128 v[164:167], v13 offset:32768
	s_waitcnt lgkmcnt(11)
	v_mfma_f32_16x16x32_bf16 v[2:5], v[120:123], v[66:69], 0
	ds_read_b128 v[120:123], v10 offset:36864
	s_waitcnt lgkmcnt(11)
	v_mfma_f32_16x16x32_bf16 v[2:5], v[124:127], v[62:65], v[2:5]
	ds_read_b128 v[124:127], v11 offset:36864
	s_waitcnt lgkmcnt(11)
	v_mfma_f32_16x16x32_bf16 v[2:5], v[128:131], v[58:61], v[2:5]
	ds_read_b128 v[128:131], v12 offset:36864
	s_waitcnt lgkmcnt(11)
	v_mfma_f32_16x16x32_bf16 v[22:25], v[132:135], v[54:57], v[2:5]
	ds_read_b128 v[132:135], v13 offset:36864
	s_waitcnt lgkmcnt(11)
	v_mfma_f32_16x16x32_bf16 v[6:9], v[136:139], v[66:69], 0
	s_waitcnt lgkmcnt(10)
	v_mfma_f32_16x16x32_bf16 v[6:9], v[140:143], v[62:65], v[6:9]
	s_waitcnt lgkmcnt(9)
	v_mfma_f32_16x16x32_bf16 v[6:9], v[144:147], v[58:61], v[6:9]
	s_waitcnt lgkmcnt(8)
	v_mfma_f32_16x16x32_bf16 v[18:21], v[148:151], v[54:57], v[6:9]
	s_waitcnt lgkmcnt(7)
	v_mfma_f32_16x16x32_bf16 v[2:5], v[152:155], v[66:69], 0
	s_waitcnt lgkmcnt(6)
	v_mfma_f32_16x16x32_bf16 v[2:5], v[156:159], v[62:65], v[2:5]
	s_waitcnt lgkmcnt(5)
	v_mfma_f32_16x16x32_bf16 v[2:5], v[160:163], v[58:61], v[2:5]
	s_waitcnt lgkmcnt(4)
	v_mfma_f32_16x16x32_bf16 v[50:53], v[164:167], v[54:57], v[2:5]
	s_waitcnt lgkmcnt(3)
	v_mfma_f32_16x16x32_bf16 v[6:9], v[120:123], v[66:69], 0
	s_waitcnt lgkmcnt(2)
	v_mfma_f32_16x16x32_bf16 v[6:9], v[124:127], v[62:65], v[6:9]
	s_waitcnt lgkmcnt(1)
	v_mfma_f32_16x16x32_bf16 v[6:9], v[128:131], v[58:61], v[6:9]
	s_waitcnt lgkmcnt(0)
	s_barrier
; #define ATT_BAR() do { asm volatile("" ::: "memory"); __builtin_amdgcn_s_barrier(); asm volatile("" ::: "memory"); } while (0)
; __device__ __forceinline__ void att_issue(Frame& F, const bf16* T_, const AttU& c, unsigned lrow3k, unsigned chunk, int tile_off, int wid) {
;     const char* base = (const char*)(T_ + (size_t)c.b * SEQ * AW + c.h * HD) + (size_t)c.rho * (AW * 2);
;     const unsigned ldsb = (unsigned)(size_t)(F.lds + tile_off) + (unsigned)wid * 1024u;
;     const unsigned voff = (lrow3k << c.dsh) + chunk;
;     const int kap0 = 128 * (c.n - 1);
; #pragma unroll
;     for (int r = 0; r < 8; ++r) { const int kb = kap0 + 32 * r + ((c.n == 0 && r < 4) ? 128 : 0);
;         glds1(voff, base + ((size_t)kb << c.dsh) * (AW * 2), ldsb + r * 8192); }
; }
; __device__ __forceinline__ void att_load_q(bf16x8_t (&q)[4], const void* p) {
;     asm volatile("global_load_dwordx4 %0, %4, off\n\tglobal_load_dwordx4 %1, %4, off offset:64\n\tglobal_load_dwordx4 %2, %4, off offset:128\n\tglobal_load_dwordx4 %3, %4, off offset:192"
;                  : "=&v"(q[0]), "=&v"(q[1]), "=&v"(q[2]), "=&v"(q[3]) : "v"(p) : "memory");
; }
; __device__ __forceinline__ void phase3_attn(Frame& F, const Args& a) {
;     ...
;         asm volatile("s_waitcnt lgkmcnt(0)" ::: "memory");
;         ATT_BAR();
;         att_issue(F, Kb, cn, k3k, kch, ATT_K_OFF, wid);
;         const int tqn = ((128 * cn.n + qi) << cn.dsh) + cn.rho;
;         att_load_q(qn, (const bf16x8_t*)(Q + ((size_t)(cn.b * SEQ + tqn) * AW + cn.h * HD)) + fq);
;         const int klo = (cu.n > 0) ? qi : (qi > 128 ? qi : 128), khi = qi + 128;
;         const int kk0 = 16 * kt0 + 4 * fq;
; #pragma unroll
;         for (int i = 0; i < 2; ++i)
; #pragma unroll
;             for (int r = 0; r < 4; ++r) st[i][r] = (kk0 + 16 * i + r >= klo) ? st[i][r] : -1e30f;
; #pragma unroll
;         for (int i = 8; i < 10; ++i)
; #pragma unroll
;             for (int r = 0; r < 4; ++r) st[i][r] = (kk0 + 16 * i + r <= khi) ? st[i][r] : -1e30f;
;         if (cu.n == 0) {
; #pragma unroll
;             for (int i = 2; i < 8; ++i)
; #pragma unroll
;                 for (int r = 0; r < 4; ++r) st[i][r] = (kk0 + 16 * i + r >= klo) ? st[i][r] : -1e30f;
;         }
	s_waitcnt lgkmcnt(0)
	v_mfma_f32_16x16x32_bf16 v[54:57], v[132:135], v[54:57], v[6:9]
	s_nop 3
	v_lshl_or_b32 v2, v1, s1, v82
	s_mov_b32 s57, m0
	s_mov_b32 m0, s34
	s_nop 0
	global_load_lds_dwordx4 v2, s[58:59]
	s_mov_b32 m0, s57
	s_add_i32 s58, s64, 0xffffffa0
	s_ashr_i32 s59, s58, 31
	s_lshl_b64 s[58:59], s[58:59], s1
	s_mul_i32 s57, s59, 0xc00
	s_mul_hi_u32 s59, s58, 0xc00
	s_add_i32 s57, s59, s57
	s_mulk_i32 s58, 0xc00
	s_add_u32 s60, s80, s58
	s_addc_u32 s61, s81, s57
	s_mov_b32 s59, m0
	s_mov_b32 m0, s35
	s_nop 0
	global_load_lds_dwordx4 v2, s[60:61]
	s_mov_b32 m0, s59
	s_sub_i32 s60, s64, 64
	s_ashr_i32 s61, s60, 31
	s_lshl_b64 s[60:61], s[60:61], s1
	s_mul_i32 s59, s61, 0xc00
	s_mul_hi_u32 s61, s60, 0xc00
	s_add_i32 s59, s61, s59
	s_mulk_i32 s60, 0xc00
	s_add_u32 s62, s80, s60
	s_addc_u32 s63, s81, s59
	s_mov_b32 s61, m0
	s_mov_b32 m0, s36
	s_nop 0
	global_load_lds_dwordx4 v2, s[62:63]
	s_mov_b32 m0, s61
	s_sub_i32 s62, s64, 32
	s_ashr_i32 s63, s62, 31
	s_lshl_b64 s[62:63], s[62:63], s1
	s_mul_i32 s61, s63, 0xc00
	s_mul_hi_u32 s63, s62, 0xc00
	s_add_i32 s61, s63, s61
	s_mulk_i32 s62, 0xc00
	s_add_u32 s64, s80, s62
	s_addc_u32 s65, s81, s61
	s_mov_b32 s63, m0
	s_mov_b32 m0, s37
	s_nop 0
	global_load_lds_dwordx4 v2, s[64:65]
	s_mov_b32 m0, s63
	s_lshl_b64 s[64:65], s[96:97], s1
	s_mul_i32 s63, s65, 0xc00
	s_mul_hi_u32 s65, s64, 0xc00
	s_add_i32 s63, s65, s63
	s_mulk_i32 s64, 0xc00
	s_add_u32 s66, s80, s64
	s_addc_u32 s67, s81, s63
	s_mov_b32 s65, m0
	s_mov_b32 m0, s38
	s_nop 0
	global_load_lds_dwordx4 v2, s[66:67]
	s_mov_b32 m0, s65
	s_or_b32 s66, s96, 32
	s_mov_b32 s67, s97
	s_lshl_b64 s[66:67], s[66:67], s1
	s_mul_i32 s65, s67, 0xc00
	s_mul_hi_u32 s67, s66, 0xc00
	s_add_i32 s65, s67, s65
	s_mulk_i32 s66, 0xc00
	s_add_u32 s68, s80, s66
	s_addc_u32 s69, s81, s65
	s_mov_b32 s67, m0
	s_mov_b32 m0, s39
	s_nop 0
	global_load_lds_dwordx4 v2, s[68:69]
	s_mov_b32 m0, s67
	s_or_b32 s68, s96, 64
	s_mov_b32 s69, s97
	s_lshl_b64 s[68:69], s[68:69], s1
	s_mul_i32 s67, s69, 0xc00
	s_mul_hi_u32 s69, s68, 0xc00
	s_add_i32 s67, s69, s67
	s_mulk_i32 s68, 0xc00
	s_add_u32 s92, s80, s68
	s_addc_u32 s93, s81, s67
	s_mov_b32 s69, m0
	s_mov_b32 m0, s40
	s_nop 0
	global_load_lds_dwordx4 v2, s[92:93]
	s_mov_b32 m0, s69
	s_or_b32 s92, s96, 0x60
	s_mov_b32 s93, s97
	s_lshl_b64 s[92:93], s[92:93], s1
	s_mul_i32 s69, s93, 0xc00
	s_mul_hi_u32 s84, s92, 0xc00
	s_add_i32 s69, s84, s69
	s_mulk_i32 s92, 0xc00
	s_add_u32 s80, s80, s92
	s_addc_u32 s81, s81, s69
	s_mov_b32 s84, m0
	s_mov_b32 m0, s41
	s_nop 0
	global_load_lds_dwordx4 v2, s[80:81]
	s_mov_b32 m0, s84
	v_add_u32_e32 v2, s96, v85
	v_lshlrev_b32_e32 v2, s1, v2
	v_add_u32_e32 v66, s23, v2
	v_lshl_add_u32 v4, s51, 12, v66
	v_mov_b64_e32 v[2:3], s[82:83]
	v_mad_i64_i32 v[2:3], s[80:81], v4, s30, v[2:3]
	v_lshl_add_u64 v[2:3], v[2:3], 0, s[20:21]
	v_lshl_add_u64 v[58:59], v[2:3], 0, v[70:71]
	global_load_dwordx4 v[14:17], v[58:59], off
	global_load_dwordx4 v[10:13], v[58:59], off offset:64
	global_load_dwordx4 v[6:9], v[58:59], off offset:128
	global_load_dwordx4 v[2:5], v[58:59], off offset:192
	s_cmp_eq_u32 s22, 0
	s_cselect_b64 vcc, -1, 0
	s_cmp_lg_u32 s22, 0
	s_cbranch_scc1 .LBB0_416
	v_readlane_b32 s22, v251, 43
	v_readlane_b32 s23, v251, 44
	s_nop 1
	v_cndmask_b32_e64 v38, v38, v110, s[22:23]
	v_readlane_b32 s22, v251, 45
	v_readlane_b32 s23, v251, 46
	s_nop 1
	v_cndmask_b32_e64 v39, v39, v110, s[22:23]
	v_readlane_b32 s22, v251, 47
	v_readlane_b32 s23, v251, 48
	s_nop 1
	v_cndmask_b32_e64 v40, v40, v110, s[22:23]
	v_readlane_b32 s22, v251, 49
	v_readlane_b32 s23, v251, 50
	s_nop 1
	v_cndmask_b32_e64 v41, v41, v110, s[22:23]
	v_readlane_b32 s22, v251, 41
	v_readlane_b32 s23, v251, 42
	s_nop 1
	v_cndmask_b32_e64 v34, v34, v110, s[22:23]
	v_readlane_b32 s22, v251, 60
	v_readlane_b32 s23, v251, 61
	s_nop 1
	v_cndmask_b32_e64 v35, v35, v110, s[22:23]
	v_readlane_b32 s22, v251, 62
	v_readlane_b32 s23, v251, 63
	s_nop 1
	v_cndmask_b32_e64 v36, v36, v110, s[22:23]
	v_readlane_b32 s22, v250, 0
	v_readlane_b32 s23, v250, 1
	s_nop 1
	v_cndmask_b32_e64 v37, v37, v110, s[22:23]
	v_readlane_b32 s22, v250, 2
	v_readlane_b32 s23, v250, 3
	s_nop 1
	v_cndmask_b32_e64 v30, v30, v110, s[22:23]
	v_readlane_b32 s22, v250, 4
	v_readlane_b32 s23, v250, 5
	s_nop 1
	v_cndmask_b32_e64 v31, v31, v110, s[22:23]
	v_readlane_b32 s22, v250, 6
	v_readlane_b32 s23, v250, 7
	s_nop 1
	v_cndmask_b32_e64 v32, v32, v110, s[22:23]
	v_readlane_b32 s22, v250, 8
	v_readlane_b32 s23, v250, 9
	s_nop 1
	v_cndmask_b32_e64 v33, v33, v110, s[22:23]
	v_readlane_b32 s22, v250, 10
	v_readlane_b32 s23, v250, 11
	s_nop 1
	v_cndmask_b32_e64 v26, v26, v110, s[22:23]
	v_readlane_b32 s22, v250, 12
	v_readlane_b32 s23, v250, 13
	s_nop 1
	v_cndmask_b32_e64 v27, v27, v110, s[22:23]
	v_readlane_b32 s22, v250, 14
	v_readlane_b32 s23, v250, 15
	s_nop 1
	v_cndmask_b32_e64 v28, v28, v110, s[22:23]
	v_readlane_b32 s22, v250, 16
	v_readlane_b32 s23, v250, 17
	s_nop 1
	v_cndmask_b32_e64 v29, v29, v110, s[22:23]
	v_readlane_b32 s22, v250, 18
	v_readlane_b32 s23, v250, 19
	s_nop 1
	v_cndmask_b32_e64 v22, v22, v110, s[22:23]
	v_readlane_b32 s22, v250, 20
	v_readlane_b32 s23, v250, 21
	s_nop 1
	v_cndmask_b32_e64 v23, v23, v110, s[22:23]
	v_readlane_b32 s22, v250, 22
	v_readlane_b32 s23, v250, 23
	s_nop 1
	v_cndmask_b32_e64 v24, v24, v110, s[22:23]
	v_readlane_b32 s22, v250, 24
	v_readlane_b32 s23, v250, 25
	s_nop 1
	v_cndmask_b32_e64 v25, v25, v110, s[22:23]
	v_readlane_b32 s22, v250, 26
	v_readlane_b32 s23, v250, 27
	s_nop 1
	v_cndmask_b32_e64 v18, v18, v110, s[22:23]
	v_readlane_b32 s22, v250, 28
	v_readlane_b32 s23, v250, 29
	s_nop 1
	v_cndmask_b32_e64 v19, v19, v110, s[22:23]
	v_readlane_b32 s22, v250, 30
	v_readlane_b32 s23, v250, 31
	s_nop 1
	v_cndmask_b32_e64 v20, v20, v110, s[22:23]
	v_readlane_b32 s22, v250, 32
	v_readlane_b32 s23, v250, 33
	s_nop 1
	v_cndmask_b32_e64 v21, v21, v110, s[22:23]

; #define LAS __attribute__((address_space(3)))
; __device__ __forceinline__ int pi16(int k) { return (k & ~12) | ((k & 4) << 1) | ((k & 8) >> 1); }
; __device__ __forceinline__ int fswz(int R) { return ((R & 3) << 2) | ((R >> 2) & 3); }
; __device__ __forceinline__ void phase3_attn(Frame& F, const Args& a) {
;     ...
;         const int q4 = (lane >> 2) & 3, p4 = lane & 3, R0 = pi16(4 * fq + q4), fz = fswz(R0);
;         const int vb0 = ATT_V_OFF + (kt0 * 16 + R0) * 256 + 8 * (p4 & 1);
;         f32x4 o[8];
; #pragma unroll
;         for (int dt = 0; dt < 8; ++dt) {
;             const int vb = vb0 + ((((2 * dt) ^ (fz & 14)) | ((p4 >> 1) ^ (fz & 1))) << 4);
;             o[dt] = (f32x4){0.f, 0.f, 0.f, 0.f};
; #pragma unroll
;             for (int i2 = 0; i2 < 5; ++i2) {
;                 const s16x4 lo = __builtin_bit_cast(s16x4, __builtin_amdgcn_ds_read_tr16_b64_v4i16((LAS v4i16_t*)(F.lds + vb + (2 * i2) * 4096)));
;                 const s16x4 hi = __builtin_bit_cast(s16x4, __builtin_amdgcn_ds_read_tr16_b64_v4i16((LAS v4i16_t*)(F.lds + vb + (2 * i2 + 1) * 4096)));
;                 const bf16x8_t vf = __builtin_shufflevector(lo, hi, 0, 1, 2, 3, 4, 5, 6, 7);
;                 o[dt] = __builtin_amdgcn_mfma_f32_16x16x32_bf16(vf, pb[i2], o[dt], 0, 0, 0);
;             }
;         }
.LBB0_420:
	s_barrier
	v_add_u32_e32 v116, v102, v101
	s_waitcnt lgkmcnt(0)
	v_add_f32_e32 v68, v18, v19
	ds_read_b64_tr_b16 v[120:121], v116
	ds_read_b64_tr_b16 v[122:123], v116 offset:4096
	ds_read_b64_tr_b16 v[124:125], v116 offset:8192
	ds_read_b64_tr_b16 v[126:127], v116 offset:12288
	ds_read_b64_tr_b16 v[128:129], v116 offset:16384
	ds_read_b64_tr_b16 v[130:131], v116 offset:20480
	ds_read_b64_tr_b16 v[132:133], v116 offset:24576
	ds_read_b64_tr_b16 v[134:135], v116 offset:28672
	ds_read_b64_tr_b16 v[136:137], v116 offset:32768
	ds_read_b64_tr_b16 v[138:139], v116 offset:36864
	ds_read_b64_tr_b16 v[140:141], v103
	ds_read_b64_tr_b16 v[142:143], v103 offset:4096
	ds_read_b64_tr_b16 v[144:145], v103 offset:8192
	ds_read_b64_tr_b16 v[146:147], v103 offset:12288
	v_ashrrev_i32_e32 v73, 31, v72
	v_mov_b32_e32 v77, v71
	v_mov_b32_e32 v79, v71
	v_mov_b32_e32 v81, v71
	s_add_u32 s22, s26, s95
	s_waitcnt lgkmcnt(12)
	v_mfma_f32_16x16x32_bf16 v[18:21], v[120:123], v[42:45], 0
	ds_read_b64_tr_b16 v[120:121], v103 offset:16384
	ds_read_b64_tr_b16 v[122:123], v103 offset:20480
	s_addc_u32 s23, s27, s89
	s_waitcnt lgkmcnt(12)
	v_mfma_f32_16x16x32_bf16 v[18:21], v[124:127], v[34:37], v[18:21]
	ds_read_b64_tr_b16 v[124:125], v103 offset:24576
	ds_read_b64_tr_b16 v[126:127], v103 offset:28672
	s_add_u32 s20, s22, s20
	s_waitcnt lgkmcnt(12)
	v_mfma_f32_16x16x32_bf16 v[18:21], v[128:131], v[30:33], v[18:21]
	ds_read_b64_tr_b16 v[128:129], v103 offset:32768
	ds_read_b64_tr_b16 v[130:131], v103 offset:36864
	s_addc_u32 s21, s23, s21
	s_waitcnt lgkmcnt(12)
	v_mfma_f32_16x16x32_bf16 v[18:21], v[132:135], v[26:29], v[18:21]
	ds_read_b64_tr_b16 v[132:133], v104
	ds_read_b64_tr_b16 v[134:135], v104 offset:4096
	s_add_u32 s22, s20, s54
	s_waitcnt lgkmcnt(12)
	v_mfma_f32_16x16x32_bf16 v[18:21], v[136:139], v[22:25], v[18:21]
	ds_read_b64_tr_b16 v[136:137], v104 offset:8192
	ds_read_b64_tr_b16 v[138:139], v104 offset:12288
	s_addc_u32 s23, s21, 0
	s_waitcnt lgkmcnt(12)
	v_mfma_f32_16x16x32_bf16 v[38:41], v[140:143], v[42:45], 0
	ds_read_b64_tr_b16 v[140:141], v104 offset:16384
	ds_read_b64_tr_b16 v[142:143], v104 offset:20480
	s_add_u32 s20, s22, s56
	s_waitcnt lgkmcnt(12)
	v_mfma_f32_16x16x32_bf16 v[38:41], v[144:147], v[34:37], v[38:41]
	ds_read_b64_tr_b16 v[144:145], v104 offset:24576
	ds_read_b64_tr_b16 v[146:147], v104 offset:28672
	s_addc_u32 s21, s23, s55
	s_waitcnt lgkmcnt(12)
	v_mfma_f32_16x16x32_bf16 v[38:41], v[120:123], v[30:33], v[38:41]
	ds_read_b64_tr_b16 v[120:121], v104 offset:32768
	ds_read_b64_tr_b16 v[122:123], v104 offset:36864
	s_waitcnt lgkmcnt(12)
	v_mfma_f32_16x16x32_bf16 v[38:41], v[124:127], v[26:29], v[38:41]
	ds_read_b64_tr_b16 v[124:125], v105
	ds_read_b64_tr_b16 v[126:127], v105 offset:4096
	s_waitcnt lgkmcnt(12)
	v_mfma_f32_16x16x32_bf16 v[38:41], v[128:131], v[22:25], v[38:41]
	ds_read_b64_tr_b16 v[128:129], v105 offset:8192
	ds_read_b64_tr_b16 v[130:131], v105 offset:12288
	s_waitcnt lgkmcnt(12)
	v_mfma_f32_16x16x32_bf16 v[46:49], v[132:135], v[42:45], 0
	ds_read_b64_tr_b16 v[132:133], v105 offset:16384
	ds_read_b64_tr_b16 v[134:135], v105 offset:20480
	s_waitcnt lgkmcnt(12)
	v_mfma_f32_16x16x32_bf16 v[46:49], v[136:139], v[34:37], v[46:49]
	ds_read_b64_tr_b16 v[136:137], v105 offset:24576
	ds_read_b64_tr_b16 v[138:139], v105 offset:28672
	s_waitcnt lgkmcnt(12)
	v_mfma_f32_16x16x32_bf16 v[46:49], v[140:143], v[30:33], v[46:49]
	ds_read_b64_tr_b16 v[140:141], v105 offset:32768
	ds_read_b64_tr_b16 v[142:143], v105 offset:36864
	s_waitcnt lgkmcnt(12)
	v_mfma_f32_16x16x32_bf16 v[46:49], v[144:147], v[26:29], v[46:49]
	ds_read_b64_tr_b16 v[144:145], v106
	ds_read_b64_tr_b16 v[146:147], v106 offset:4096
	s_waitcnt lgkmcnt(12)
	v_mfma_f32_16x16x32_bf16 v[46:49], v[120:123], v[22:25], v[46:49]
	ds_read_b64_tr_b16 v[120:121], v106 offset:8192
	ds_read_b64_tr_b16 v[122:123], v106 offset:12288
	s_waitcnt lgkmcnt(12)
	v_mfma_f32_16x16x32_bf16 v[50:53], v[124:127], v[42:45], 0
	ds_read_b64_tr_b16 v[124:125], v106 offset:16384
	ds_read_b64_tr_b16 v[126:127], v106 offset:20480
	s_waitcnt lgkmcnt(12)
	v_mfma_f32_16x16x32_bf16 v[50:53], v[128:131], v[34:37], v[50:53]
	ds_read_b64_tr_b16 v[128:129], v106 offset:24576
	ds_read_b64_tr_b16 v[130:131], v106 offset:28672
	s_waitcnt lgkmcnt(12)
	v_mfma_f32_16x16x32_bf16 v[50:53], v[132:135], v[30:33], v[50:53]
	ds_read_b64_tr_b16 v[132:133], v106 offset:32768
	ds_read_b64_tr_b16 v[134:135], v106 offset:36864
	s_waitcnt lgkmcnt(12)
	v_mfma_f32_16x16x32_bf16 v[50:53], v[136:139], v[26:29], v[50:53]
	ds_read_b64_tr_b16 v[136:137], v107
	ds_read_b64_tr_b16 v[138:139], v107 offset:4096
	s_waitcnt lgkmcnt(12)
	v_mfma_f32_16x16x32_bf16 v[50:53], v[140:143], v[22:25], v[50:53]
	ds_read_b64_tr_b16 v[140:141], v107 offset:8192
	ds_read_b64_tr_b16 v[142:143], v107 offset:12288
	s_waitcnt lgkmcnt(12)
	v_mfma_f32_16x16x32_bf16 v[54:57], v[144:147], v[42:45], 0
	ds_read_b64_tr_b16 v[144:145], v107 offset:16384
	ds_read_b64_tr_b16 v[146:147], v107 offset:20480
	s_waitcnt lgkmcnt(12)
	v_mfma_f32_16x16x32_bf16 v[54:57], v[120:123], v[34:37], v[54:57]
	ds_read_b64_tr_b16 v[120:121], v107 offset:24576
	ds_read_b64_tr_b16 v[122:123], v107 offset:28672
	s_waitcnt lgkmcnt(12)
	v_mfma_f32_16x16x32_bf16 v[54:57], v[124:127], v[30:33], v[54:57]
	ds_read_b64_tr_b16 v[124:125], v107 offset:32768
	ds_read_b64_tr_b16 v[126:127], v107 offset:36864
	s_waitcnt lgkmcnt(12)
	v_mfma_f32_16x16x32_bf16 v[54:57], v[128:131], v[26:29], v[54:57]
	ds_read_b64_tr_b16 v[128:129], v108
	ds_read_b64_tr_b16 v[130:131], v108 offset:4096
	s_waitcnt lgkmcnt(12)
; __device__ __forceinline__ unsigned cvt_pk_bf16(float lo, float hi) { unsigned r; asm volatile("v_cvt_pk_bf16_f32 %0, %1, %2" : "=v"(r) : "v"(lo), "v"(hi)); return r; }
; __device__ __forceinline__ void swap16(int& x, int& y) { const auto r = __builtin_amdgcn_permlane16_swap((unsigned)x, (unsigned)y, false, false); x = (int)r[0]; y = (int)r[1]; }
; #define ATT_BAR() do { asm volatile("" ::: "memory"); __builtin_amdgcn_s_barrier(); asm volatile("" ::: "memory"); } while (0)
; __device__ __forceinline__ void att_issue(Frame& F, const bf16* T_, const AttU& c, unsigned lrow3k, unsigned chunk, int tile_off, int wid) {
;     const char* base = (const char*)(T_ + (size_t)c.b * SEQ * AW + c.h * HD) + (size_t)c.rho * (AW * 2);
;     const unsigned ldsb = (unsigned)(size_t)(F.lds + tile_off) + (unsigned)wid * 1024u;
;     const unsigned voff = (lrow3k << c.dsh) + chunk;
;     const int kap0 = 128 * (c.n - 1);
; #pragma unroll
;     for (int r = 0; r < 8; ++r) { const int kb = kap0 + 32 * r + ((c.n == 0 && r < 4) ? 128 : 0);
;         glds1(voff, base + ((size_t)kb << c.dsh) * (AW * 2), ldsb + r * 8192); }
; }
; __device__ __forceinline__ void phase3_attn(Frame& F, const Args& a) {
;     ...
;         }
;         asm volatile("s_waitcnt lgkmcnt(0)" ::: "memory");
;         ATT_BAR();
;         att_issue(F, Vb, cn, v3k, vch, ATT_V_OFF, wid);
;         const float inv = 1.0f / l;
;         bf16* orow = OP + ((size_t)cu.br * T + (size_t)cu.b * SEQ + tq) * AW + cu.h * HD + 4 * fq;
; #pragma unroll
;         for (int d2 = 0; d2 < 4; ++d2) {
;             int x0 = (int)pg8::cvt_pk_bf16(o[2 * d2][0] * inv, o[2 * d2][1] * inv), x1 = (int)pg8::cvt_pk_bf16(o[2 * d2][2] * inv, o[2 * d2][3] * inv);
;             int y0 = (int)pg8::cvt_pk_bf16(o[2 * d2 + 1][0] * inv, o[2 * d2 + 1][1] * inv), y1 = (int)pg8::cvt_pk_bf16(o[2 * d2 + 1][2] * inv, o[2 * d2 + 1][3] * inv);
;             pg8::swap16(x0, y0); pg8::swap16(x1, y1);
;             v4u w; w.x = (unsigned)x0; w.y = (unsigned)x1; w.z = (unsigned)y0; w.w = (unsigned)y1;
;             *(v4u*)(orow + 16 * (2 * d2 + (fq & 1)) - 4 * (fq & 1)) = w; }
;         { float* lp = LSE + ((size_t)cu.br * T + (size_t)cu.b * SEQ + tq) * NH + cu.h; const float lv = mx + __log2f(l); if (fq == 0) *lp = lv; }
	v_mfma_f32_16x16x32_bf16 v[54:57], v[132:135], v[22:25], v[54:57]
	ds_read_b64_tr_b16 v[132:133], v108 offset:8192
	ds_read_b64_tr_b16 v[134:135], v108 offset:12288
	s_waitcnt lgkmcnt(12)
	v_mfma_f32_16x16x32_bf16 v[58:61], v[136:139], v[42:45], 0
	ds_read_b64_tr_b16 v[136:137], v108 offset:16384
	ds_read_b64_tr_b16 v[138:139], v108 offset:20480
	s_waitcnt lgkmcnt(12)
	v_mfma_f32_16x16x32_bf16 v[58:61], v[140:143], v[34:37], v[58:61]
	ds_read_b64_tr_b16 v[140:141], v108 offset:24576
	ds_read_b64_tr_b16 v[142:143], v108 offset:28672
	s_waitcnt lgkmcnt(12)
	v_mfma_f32_16x16x32_bf16 v[58:61], v[144:147], v[30:33], v[58:61]
	ds_read_b64_tr_b16 v[144:145], v108 offset:32768
	ds_read_b64_tr_b16 v[146:147], v108 offset:36864
	s_waitcnt lgkmcnt(12)
	v_mfma_f32_16x16x32_bf16 v[58:61], v[120:123], v[26:29], v[58:61]
	ds_read_b64_tr_b16 v[120:121], v109
	ds_read_b64_tr_b16 v[122:123], v109 offset:4096
	s_waitcnt lgkmcnt(12)
	v_mfma_f32_16x16x32_bf16 v[58:61], v[124:127], v[22:25], v[58:61]
	ds_read_b64_tr_b16 v[124:125], v109 offset:8192
	ds_read_b64_tr_b16 v[126:127], v109 offset:12288
	s_waitcnt lgkmcnt(12)
	v_mfma_f32_16x16x32_bf16 v[62:65], v[128:131], v[42:45], 0
	ds_read_b64_tr_b16 v[128:129], v109 offset:16384
	ds_read_b64_tr_b16 v[130:131], v109 offset:20480
	s_waitcnt lgkmcnt(12)
	v_mfma_f32_16x16x32_bf16 v[62:65], v[132:135], v[34:37], v[62:65]
	ds_read_b64_tr_b16 v[132:133], v109 offset:24576
	ds_read_b64_tr_b16 v[134:135], v109 offset:28672
	s_waitcnt lgkmcnt(12)
	v_mfma_f32_16x16x32_bf16 v[62:65], v[136:139], v[30:33], v[62:65]
	ds_read_b64_tr_b16 v[136:137], v109 offset:32768
	ds_read_b64_tr_b16 v[138:139], v109 offset:36864
	s_waitcnt lgkmcnt(12)
	v_mfma_f32_16x16x32_bf16 v[62:65], v[140:143], v[26:29], v[62:65]
	s_waitcnt lgkmcnt(10)
	v_mfma_f32_16x16x32_bf16 v[62:65], v[144:147], v[22:25], v[62:65]
	s_waitcnt lgkmcnt(8)
	v_mfma_f32_16x16x32_bf16 v[112:115], v[120:123], v[42:45], 0
	s_waitcnt lgkmcnt(6)
	v_mfma_f32_16x16x32_bf16 v[112:115], v[124:127], v[34:37], v[112:115]
	s_waitcnt lgkmcnt(4)
	v_mfma_f32_16x16x32_bf16 v[112:115], v[128:131], v[30:33], v[112:115]
	s_waitcnt lgkmcnt(2)
	v_mfma_f32_16x16x32_bf16 v[112:115], v[132:135], v[26:29], v[112:115]
	s_waitcnt lgkmcnt(0)
	s_barrier
	s_waitcnt lgkmcnt(0)
	v_mfma_f32_16x16x32_bf16 v[22:25], v[136:139], v[22:25], v[112:115]
	s_nop 2
	v_lshl_or_b32 v26, v83, s1, v84
	s_mov_b32 s1, m0
	s_mov_b32 m0, s42
	s_nop 0
	global_load_lds_dwordx4 v26, s[20:21]
	s_mov_b32 m0, s1
	s_add_u32 s20, s22, s58
	s_addc_u32 s21, s23, s57
	s_mov_b32 s1, m0
	s_mov_b32 m0, s43
	s_nop 0
	global_load_lds_dwordx4 v26, s[20:21]
	s_mov_b32 m0, s1
	s_add_u32 s20, s22, s60
	s_addc_u32 s21, s23, s59
	s_mov_b32 s1, m0
	s_mov_b32 m0, s44
	s_nop 0
	global_load_lds_dwordx4 v26, s[20:21]
	s_mov_b32 m0, s1
	s_add_u32 s20, s22, s62
	s_addc_u32 s21, s23, s61
	s_mov_b32 s1, m0
	s_mov_b32 m0, s45
	s_nop 0
	global_load_lds_dwordx4 v26, s[20:21]
	s_mov_b32 m0, s1
	s_add_u32 s20, s22, s64
	s_addc_u32 s21, s23, s63
	s_mov_b32 s1, m0
	s_mov_b32 m0, s46
	s_nop 0
	global_load_lds_dwordx4 v26, s[20:21]
	s_mov_b32 m0, s1
	s_add_u32 s20, s22, s66
	s_addc_u32 s21, s23, s65
	s_mov_b32 s1, m0
	s_mov_b32 m0, s47
	s_nop 0
	global_load_lds_dwordx4 v26, s[20:21]
	s_mov_b32 m0, s1
	s_add_u32 s20, s22, s68
	s_addc_u32 s21, s23, s67
	s_mov_b32 s1, m0
	s_mov_b32 m0, s48
	s_nop 0
	global_load_lds_dwordx4 v26, s[20:21]
	s_mov_b32 m0, s1
	s_add_u32 s20, s22, s92
	s_addc_u32 s21, s23, s69
	s_mov_b32 s1, m0
	s_mov_b32 m0, s49
	s_nop 0
	global_load_lds_dwordx4 v26, s[20:21]
	s_mov_b32 m0, s1
	v_div_scale_f32 v26, s[20:21], v68, v68, 1.0
	v_rcp_f32_e32 v27, v26
	s_ashr_i32 s1, s0, 31
	s_ashr_i32 s89, s88, 31
	s_lshl_b64 s[0:1], s[0:1], 14
	v_fma_f32 v28, -v26, v27, 1.0
	v_fmac_f32_e32 v27, v28, v27
	v_div_scale_f32 v28, vcc, 1.0, v68, 1.0
	v_mul_f32_e32 v29, v28, v27
	v_fma_f32 v30, -v26, v29, v28
	v_fmac_f32_e32 v29, v30, v27
	s_lshl_b64 s[20:21], s[88:89], 12
	v_fma_f32 v26, -v26, v29, v28
	s_add_u32 s0, s0, s20
	v_div_fmas_f32 v26, v26, v27, v29
	s_addc_u32 s1, s1, s21
	v_div_fixup_f32 v32, v26, v68, 1.0
	v_lshl_add_u64 v[26:27], s[0:1], 0, v[72:73]
	v_mov_b64_e32 v[28:29], s[90:91]
	v_mad_u64_u32 v[28:29], s[0:1], v26, s30, v[28:29]
	s_lshl_b32 s0, s94, 7
	v_mul_f32_e32 v18, v32, v18
	v_mul_f32_e32 v19, v32, v19
	v_mad_i32_i24 v29, v27, s30, v29
	s_ashr_i32 s1, s0, 31
	v_cvt_pk_bf16_f32 v18, v18, v19
	v_mul_f32_e32 v19, v32, v20
	v_mul_f32_e32 v20, v32, v21
	v_lshl_add_u64 v[28:29], s[0:1], 1, v[28:29]
	v_cvt_pk_bf16_f32 v19, v19, v20
	v_mul_f32_e32 v20, v32, v38
	v_mul_f32_e32 v21, v32, v39
	v_lshl_add_u64 v[28:29], v[28:29], 0, v[76:77]
	v_cvt_pk_bf16_f32 v20, v20, v21
	v_mul_f32_e32 v21, v32, v40
	v_lshl_add_u64 v[28:29], v[74:75], 1, v[28:29]
	v_mul_f32_e32 v30, v32, v41
	v_cvt_pk_bf16_f32 v21, v21, v30
	v_permlane16_swap_b32_e32 v18, v20
	v_permlane16_swap_b32_e32 v19, v21
	v_lshl_add_u64 v[30:31], v[28:29], 0, v[78:79]
	global_store_dwordx4 v[30:31], v[18:21], off
	v_mul_f32_e32 v33, v32, v53
	v_lshl_add_u64 v[28:29], v[28:29], 0, v[80:81]
	v_mul_f32_e32 v18, v32, v46
	v_mul_f32_e32 v19, v32, v47
	v_cvt_pk_bf16_f32 v18, v18, v19
	v_mul_f32_e32 v19, v32, v48
	v_mul_f32_e32 v20, v32, v49
	v_cvt_pk_bf16_f32 v19, v19, v20
	v_mul_f32_e32 v20, v32, v50
	v_mul_f32_e32 v21, v32, v51
	v_cvt_pk_bf16_f32 v20, v20, v21
	v_mul_f32_e32 v21, v32, v52
	v_cvt_pk_bf16_f32 v21, v21, v33
	v_permlane16_swap_b32_e32 v18, v20
	s_nop 0
	v_permlane16_swap_b32_e32 v19, v21
	global_store_dwordx4 v[28:29], v[18:21], off offset:64
	v_mul_f32_e32 v33, v32, v61
	s_nop 0
	v_mul_f32_e32 v18, v32, v54
	v_mul_f32_e32 v19, v32, v55
	v_cvt_pk_bf16_f32 v18, v18, v19
	v_mul_f32_e32 v19, v32, v56
	v_mul_f32_e32 v20, v32, v57
	v_cvt_pk_bf16_f32 v19, v19, v20
	v_mul_f32_e32 v20, v32, v58
	v_mul_f32_e32 v21, v32, v59
	v_cvt_pk_bf16_f32 v20, v20, v21
	v_mul_f32_e32 v21, v32, v60
	v_cvt_pk_bf16_f32 v21, v21, v33
	v_permlane16_swap_b32_e32 v18, v20
	s_nop 0
	v_permlane16_swap_b32_e32 v19, v21
	global_store_dwordx4 v[30:31], v[18:21], off offset:128
	s_nop 1
	v_mul_f32_e32 v18, v32, v62
	v_mul_f32_e32 v19, v32, v63
	v_cvt_pk_bf16_f32 v18, v18, v19
	v_mul_f32_e32 v19, v32, v64
	v_mul_f32_e32 v20, v32, v65
	v_cvt_pk_bf16_f32 v19, v19, v20
	v_mul_f32_e32 v20, v32, v22
	v_mul_f32_e32 v21, v32, v23
	v_cvt_pk_bf16_f32 v20, v20, v21
	v_mul_f32_e32 v21, v32, v24
	v_mul_f32_e32 v22, v32, v25
	v_cvt_pk_bf16_f32 v21, v21, v22
	v_permlane16_swap_b32_e32 v18, v20
	v_permlane16_swap_b32_e32 v19, v21
	global_store_dwordx4 v[28:29], v[18:21], off offset:192
	s_and_saveexec_b64 s[0:1], s[2:3]
	s_cbranch_execz .LBB0_409
	v_log_f32_e32 v18, v68
	s_ashr_i32 s95, s94, 31
	v_add_f32_e32 v20, v67, v18
	v_mad_u64_u32 v[18:19], s[20:21], v26, 48, s[86:87]
	v_mad_i32_i24 v19, v27, 48, v19
	v_lshl_add_u64 v[18:19], s[94:95], 2, v[18:19]
	global_store_dword v[18:19], v20, off
	s_branch .LBB0_409
